# E27: E21 + route phase router-weight LDS reads software-pipelined 3 groups ahead into spare VGPRs (was read->wait->use serial)
# speedup vs baseline: 1.0029x; 1.0029x over previous
.LBB0_1364:
	ds_read_b128 v[194:197], v89
	ds_read_b128 v[198:201], v89 offset:1024
	ds_read_b128 v[202:205], v89 offset:2048
	ds_read_b128 v[206:209], v89 offset:3072
	v_mov_b32_e32 v44, v46
	v_mov_b32_e32 v45, v4
	v_mov_b32_e32 v4, v47
	v_mov_b32_e32 v46, v48
	s_waitcnt lgkmcnt(3)
	v_pk_fma_f32 v[66:67], v[44:45], v[194:195], 0 op_sel_hi:[1,0,0]
	v_mov_b32_e32 v47, v2
	v_pk_fma_f32 v[62:63], v[4:5], v[194:195], v[66:67] op_sel:[0,1,0]
	v_mov_b32_e32 v2, v49
	v_pk_fma_f32 v[62:63], v[46:47], v[196:197], v[62:63] op_sel_hi:[1,0,1]
	v_mov_b32_e32 v48, v197
	v_pk_fma_f32 v[66:67], v[2:3], v[48:49], v[62:63] op_sel_hi:[1,0,1]
	ds_read_b128 v[194:197], v89 offset:4096
	v_mov_b32_e32 v48, v50
	v_mov_b32_e32 v49, v12
	v_mov_b32_e32 v12, v51
	v_mov_b32_e32 v50, v52
	s_waitcnt lgkmcnt(3)
	v_pk_fma_f32 v[66:67], v[48:49], v[198:199], v[66:67] op_sel_hi:[1,0,1]
	v_mov_b32_e32 v51, v10
	v_pk_fma_f32 v[62:63], v[12:13], v[198:199], v[66:67] op_sel:[0,1,0]
	v_mov_b32_e32 v10, v53
	v_pk_fma_f32 v[62:63], v[50:51], v[200:201], v[62:63] op_sel_hi:[1,0,1]
	v_mov_b32_e32 v52, v201
	v_pk_fma_f32 v[66:67], v[10:11], v[52:53], v[62:63] op_sel_hi:[1,0,1]
	ds_read_b128 v[198:201], v89 offset:5120
	v_mov_b32_e32 v52, v54
	v_mov_b32_e32 v53, v42
	v_mov_b32_e32 v42, v55
	v_mov_b32_e32 v54, v56
	s_waitcnt lgkmcnt(3)
	v_pk_fma_f32 v[66:67], v[52:53], v[202:203], v[66:67] op_sel_hi:[1,0,1]
	v_mov_b32_e32 v55, v40
	v_pk_fma_f32 v[62:63], v[42:43], v[202:203], v[66:67] op_sel:[0,1,0]
	v_mov_b32_e32 v40, v57
	v_pk_fma_f32 v[62:63], v[54:55], v[204:205], v[62:63] op_sel_hi:[1,0,1]
	v_mov_b32_e32 v56, v205
	v_pk_fma_f32 v[66:67], v[40:41], v[56:57], v[62:63] op_sel_hi:[1,0,1]
	ds_read_b128 v[202:205], v89 offset:6144
	v_mov_b32_e32 v56, v58
	v_mov_b32_e32 v57, v8
	v_mov_b32_e32 v8, v59
	v_mov_b32_e32 v58, v60
	s_waitcnt lgkmcnt(3)
	v_pk_fma_f32 v[66:67], v[56:57], v[206:207], v[66:67] op_sel_hi:[1,0,1]
	v_mov_b32_e32 v59, v6
	v_pk_fma_f32 v[62:63], v[8:9], v[206:207], v[66:67] op_sel:[0,1,0]
	v_mov_b32_e32 v6, v61
	v_pk_fma_f32 v[62:63], v[58:59], v[208:209], v[62:63] op_sel_hi:[1,0,1]
	v_mov_b32_e32 v60, v209
	v_pk_fma_f32 v[60:61], v[6:7], v[60:61], v[62:63] op_sel_hi:[1,0,1]
	ds_read_b128 v[206:209], v89 offset:7168
	s_waitcnt lgkmcnt(3)
	v_pk_fma_f32 v[66:67], v[44:45], v[194:195], 0 op_sel_hi:[1,0,0]
	s_nop 0
	v_pk_fma_f32 v[62:63], v[4:5], v[194:195], v[66:67] op_sel:[0,1,0]
	s_nop 0
	v_pk_fma_f32 v[62:63], v[46:47], v[196:197], v[62:63] op_sel_hi:[1,0,1]
	v_mov_b32_e32 v196, v197
	v_pk_fma_f32 v[66:67], v[2:3], v[196:197], v[62:63] op_sel_hi:[1,0,1]
	ds_read_b128 v[194:197], v89 offset:8192
	s_waitcnt lgkmcnt(3)
	v_pk_fma_f32 v[66:67], v[48:49], v[198:199], v[66:67] op_sel_hi:[1,0,1]
	s_nop 0
	v_pk_fma_f32 v[62:63], v[12:13], v[198:199], v[66:67] op_sel:[0,1,0]
	s_nop 0
	v_pk_fma_f32 v[62:63], v[50:51], v[200:201], v[62:63] op_sel_hi:[1,0,1]
	v_mov_b32_e32 v200, v201
	v_pk_fma_f32 v[66:67], v[10:11], v[200:201], v[62:63] op_sel_hi:[1,0,1]
	ds_read_b128 v[198:201], v89 offset:9216
	s_waitcnt lgkmcnt(3)
	v_pk_fma_f32 v[66:67], v[52:53], v[202:203], v[66:67] op_sel_hi:[1,0,1]
	s_nop 0
	v_pk_fma_f32 v[62:63], v[42:43], v[202:203], v[66:67] op_sel:[0,1,0]
	s_nop 0
	v_pk_fma_f32 v[62:63], v[54:55], v[204:205], v[62:63] op_sel_hi:[1,0,1]
	v_mov_b32_e32 v204, v205
	v_pk_fma_f32 v[66:67], v[40:41], v[204:205], v[62:63] op_sel_hi:[1,0,1]
	ds_read_b128 v[202:205], v89 offset:10240
	s_waitcnt lgkmcnt(3)
	v_pk_fma_f32 v[66:67], v[56:57], v[206:207], v[66:67] op_sel_hi:[1,0,1]
	s_nop 0
	v_pk_fma_f32 v[62:63], v[8:9], v[206:207], v[66:67] op_sel:[0,1,0]
	s_nop 0
	v_pk_fma_f32 v[62:63], v[58:59], v[208:209], v[62:63] op_sel_hi:[1,0,1]
	v_mov_b32_e32 v208, v209
	v_pk_fma_f32 v[62:63], v[6:7], v[208:209], v[62:63] op_sel_hi:[1,0,1]
	ds_read_b128 v[206:209], v89 offset:11264
	s_waitcnt lgkmcnt(3)
	v_pk_fma_f32 v[68:69], v[44:45], v[194:195], 0 op_sel_hi:[1,0,0]
	s_nop 0
	v_pk_fma_f32 v[64:65], v[4:5], v[194:195], v[68:69] op_sel:[0,1,0]
	s_nop 0
	v_pk_fma_f32 v[64:65], v[46:47], v[196:197], v[64:65] op_sel_hi:[1,0,1]
	v_mov_b32_e32 v196, v197
	v_pk_fma_f32 v[68:69], v[2:3], v[196:197], v[64:65] op_sel_hi:[1,0,1]
	ds_read_b128 v[194:197], v89 offset:12288
	s_waitcnt lgkmcnt(3)
	v_pk_fma_f32 v[68:69], v[48:49], v[198:199], v[68:69] op_sel_hi:[1,0,1]
	s_nop 0
	v_pk_fma_f32 v[64:65], v[12:13], v[198:199], v[68:69] op_sel:[0,1,0]
	s_nop 0
	v_pk_fma_f32 v[64:65], v[50:51], v[200:201], v[64:65] op_sel_hi:[1,0,1]
	v_mov_b32_e32 v200, v201
	v_pk_fma_f32 v[68:69], v[10:11], v[200:201], v[64:65] op_sel_hi:[1,0,1]
	ds_read_b128 v[198:201], v89 offset:13312
	s_waitcnt lgkmcnt(3)
	v_pk_fma_f32 v[68:69], v[52:53], v[202:203], v[68:69] op_sel_hi:[1,0,1]
	s_nop 0
	v_pk_fma_f32 v[64:65], v[42:43], v[202:203], v[68:69] op_sel:[0,1,0]
	s_nop 0
	v_pk_fma_f32 v[64:65], v[54:55], v[204:205], v[64:65] op_sel_hi:[1,0,1]
	v_mov_b32_e32 v204, v205
	v_pk_fma_f32 v[68:69], v[40:41], v[204:205], v[64:65] op_sel_hi:[1,0,1]
	ds_read_b128 v[202:205], v89 offset:14336
	s_waitcnt lgkmcnt(3)
	v_pk_fma_f32 v[68:69], v[56:57], v[206:207], v[68:69] op_sel_hi:[1,0,1]
	s_nop 0
	v_pk_fma_f32 v[64:65], v[8:9], v[206:207], v[68:69] op_sel:[0,1,0]
	s_nop 0
	v_pk_fma_f32 v[64:65], v[58:59], v[208:209], v[64:65] op_sel_hi:[1,0,1]
	v_mov_b32_e32 v208, v209
	v_pk_fma_f32 v[64:65], v[6:7], v[208:209], v[64:65] op_sel_hi:[1,0,1]
	ds_read_b128 v[206:209], v89 offset:15360
	s_waitcnt lgkmcnt(3)
	v_pk_fma_f32 v[70:71], v[44:45], v[194:195], 0 op_sel_hi:[1,0,0]
	s_nop 0
	v_pk_fma_f32 v[66:67], v[4:5], v[194:195], v[70:71] op_sel:[0,1,0]
	s_nop 0
	v_pk_fma_f32 v[66:67], v[46:47], v[196:197], v[66:67] op_sel_hi:[1,0,1]
	v_mov_b32_e32 v196, v197
	v_pk_fma_f32 v[70:71], v[2:3], v[196:197], v[66:67] op_sel_hi:[1,0,1]
	ds_read_b128 v[194:197], v89 offset:16384
	s_waitcnt lgkmcnt(3)
	v_pk_fma_f32 v[70:71], v[48:49], v[198:199], v[70:71] op_sel_hi:[1,0,1]
	s_nop 0
	v_pk_fma_f32 v[66:67], v[12:13], v[198:199], v[70:71] op_sel:[0,1,0]
	s_nop 0
	v_pk_fma_f32 v[66:67], v[50:51], v[200:201], v[66:67] op_sel_hi:[1,0,1]
	v_mov_b32_e32 v200, v201
	v_pk_fma_f32 v[70:71], v[10:11], v[200:201], v[66:67] op_sel_hi:[1,0,1]
	ds_read_b128 v[198:201], v89 offset:17408
	s_waitcnt lgkmcnt(3)
	v_pk_fma_f32 v[70:71], v[52:53], v[202:203], v[70:71] op_sel_hi:[1,0,1]
	s_nop 0
	v_pk_fma_f32 v[66:67], v[42:43], v[202:203], v[70:71] op_sel:[0,1,0]
	s_nop 0
	v_pk_fma_f32 v[66:67], v[54:55], v[204:205], v[66:67] op_sel_hi:[1,0,1]
	v_mov_b32_e32 v204, v205
	v_pk_fma_f32 v[70:71], v[40:41], v[204:205], v[66:67] op_sel_hi:[1,0,1]
	ds_read_b128 v[202:205], v89 offset:18432
	s_waitcnt lgkmcnt(3)
	v_pk_fma_f32 v[70:71], v[56:57], v[206:207], v[70:71] op_sel_hi:[1,0,1]
	s_nop 0
	v_pk_fma_f32 v[66:67], v[8:9], v[206:207], v[70:71] op_sel:[0,1,0]
	s_nop 0
	v_pk_fma_f32 v[66:67], v[58:59], v[208:209], v[66:67] op_sel_hi:[1,0,1]
	v_mov_b32_e32 v208, v209
	v_pk_fma_f32 v[66:67], v[6:7], v[208:209], v[66:67] op_sel_hi:[1,0,1]
	ds_read_b128 v[206:209], v89 offset:19456
	s_waitcnt lgkmcnt(3)
	v_pk_fma_f32 v[72:73], v[44:45], v[194:195], 0 op_sel_hi:[1,0,0]
	s_nop 0
	v_pk_fma_f32 v[68:69], v[4:5], v[194:195], v[72:73] op_sel:[0,1,0]
	s_nop 0
	v_pk_fma_f32 v[68:69], v[46:47], v[196:197], v[68:69] op_sel_hi:[1,0,1]
	v_mov_b32_e32 v196, v197
	v_pk_fma_f32 v[72:73], v[2:3], v[196:197], v[68:69] op_sel_hi:[1,0,1]
	ds_read_b128 v[194:197], v89 offset:20480
	s_waitcnt lgkmcnt(3)
	v_pk_fma_f32 v[72:73], v[48:49], v[198:199], v[72:73] op_sel_hi:[1,0,1]
	s_nop 0
	v_pk_fma_f32 v[68:69], v[12:13], v[198:199], v[72:73] op_sel:[0,1,0]
	s_nop 0
	v_pk_fma_f32 v[68:69], v[50:51], v[200:201], v[68:69] op_sel_hi:[1,0,1]
	v_mov_b32_e32 v200, v201
	v_pk_fma_f32 v[72:73], v[10:11], v[200:201], v[68:69] op_sel_hi:[1,0,1]
	ds_read_b128 v[198:201], v89 offset:21504
	s_waitcnt lgkmcnt(3)
	v_pk_fma_f32 v[72:73], v[52:53], v[202:203], v[72:73] op_sel_hi:[1,0,1]
	s_nop 0
	v_pk_fma_f32 v[68:69], v[42:43], v[202:203], v[72:73] op_sel:[0,1,0]
	s_nop 0
	v_pk_fma_f32 v[68:69], v[54:55], v[204:205], v[68:69] op_sel_hi:[1,0,1]
	v_mov_b32_e32 v204, v205
	v_pk_fma_f32 v[72:73], v[40:41], v[204:205], v[68:69] op_sel_hi:[1,0,1]
	ds_read_b128 v[202:205], v89 offset:22528
	s_waitcnt lgkmcnt(3)
	v_pk_fma_f32 v[72:73], v[56:57], v[206:207], v[72:73] op_sel_hi:[1,0,1]
	s_nop 0
	v_pk_fma_f32 v[68:69], v[8:9], v[206:207], v[72:73] op_sel:[0,1,0]
	s_nop 0
	v_pk_fma_f32 v[68:69], v[58:59], v[208:209], v[68:69] op_sel_hi:[1,0,1]
	v_mov_b32_e32 v208, v209
	v_pk_fma_f32 v[68:69], v[6:7], v[208:209], v[68:69] op_sel_hi:[1,0,1]
	ds_read_b128 v[206:209], v89 offset:23552
	s_waitcnt lgkmcnt(3)
	v_pk_fma_f32 v[74:75], v[44:45], v[194:195], 0 op_sel_hi:[1,0,0]
	s_nop 0
	v_pk_fma_f32 v[70:71], v[4:5], v[194:195], v[74:75] op_sel:[0,1,0]
	s_nop 0
	v_pk_fma_f32 v[70:71], v[46:47], v[196:197], v[70:71] op_sel_hi:[1,0,1]
	v_mov_b32_e32 v196, v197
	v_pk_fma_f32 v[74:75], v[2:3], v[196:197], v[70:71] op_sel_hi:[1,0,1]
	ds_read_b128 v[194:197], v89 offset:24576
	s_waitcnt lgkmcnt(3)
	v_pk_fma_f32 v[74:75], v[48:49], v[198:199], v[74:75] op_sel_hi:[1,0,1]
	s_nop 0
	v_pk_fma_f32 v[70:71], v[12:13], v[198:199], v[74:75] op_sel:[0,1,0]
	s_nop 0
	v_pk_fma_f32 v[70:71], v[50:51], v[200:201], v[70:71] op_sel_hi:[1,0,1]
	v_mov_b32_e32 v200, v201
	v_pk_fma_f32 v[74:75], v[10:11], v[200:201], v[70:71] op_sel_hi:[1,0,1]
	ds_read_b128 v[198:201], v89 offset:25600
	s_waitcnt lgkmcnt(3)
	v_pk_fma_f32 v[74:75], v[52:53], v[202:203], v[74:75] op_sel_hi:[1,0,1]
	s_nop 0
	v_pk_fma_f32 v[70:71], v[42:43], v[202:203], v[74:75] op_sel:[0,1,0]
	s_nop 0
	v_pk_fma_f32 v[70:71], v[54:55], v[204:205], v[70:71] op_sel_hi:[1,0,1]
	v_mov_b32_e32 v204, v205
	v_pk_fma_f32 v[74:75], v[40:41], v[204:205], v[70:71] op_sel_hi:[1,0,1]
	ds_read_b128 v[202:205], v89 offset:26624
	s_waitcnt lgkmcnt(3)
	v_pk_fma_f32 v[74:75], v[56:57], v[206:207], v[74:75] op_sel_hi:[1,0,1]
	s_nop 0
	v_pk_fma_f32 v[70:71], v[8:9], v[206:207], v[74:75] op_sel:[0,1,0]
	s_nop 0
	v_pk_fma_f32 v[70:71], v[58:59], v[208:209], v[70:71] op_sel_hi:[1,0,1]
	v_mov_b32_e32 v208, v209
	v_pk_fma_f32 v[70:71], v[6:7], v[208:209], v[70:71] op_sel_hi:[1,0,1]
	ds_read_b128 v[206:209], v89 offset:27648
	s_waitcnt lgkmcnt(3)
	v_pk_fma_f32 v[76:77], v[44:45], v[194:195], 0 op_sel_hi:[1,0,0]
	s_nop 0
	v_pk_fma_f32 v[72:73], v[4:5], v[194:195], v[76:77] op_sel:[0,1,0]
	s_nop 0
	v_pk_fma_f32 v[72:73], v[46:47], v[196:197], v[72:73] op_sel_hi:[1,0,1]
	v_mov_b32_e32 v196, v197
	v_pk_fma_f32 v[76:77], v[2:3], v[196:197], v[72:73] op_sel_hi:[1,0,1]
	ds_read_b128 v[194:197], v89 offset:28672
	s_waitcnt lgkmcnt(3)
	v_pk_fma_f32 v[76:77], v[48:49], v[198:199], v[76:77] op_sel_hi:[1,0,1]
	s_nop 0
	v_pk_fma_f32 v[72:73], v[12:13], v[198:199], v[76:77] op_sel:[0,1,0]
	s_nop 0
	v_pk_fma_f32 v[72:73], v[50:51], v[200:201], v[72:73] op_sel_hi:[1,0,1]
	v_mov_b32_e32 v200, v201
	v_pk_fma_f32 v[76:77], v[10:11], v[200:201], v[72:73] op_sel_hi:[1,0,1]
	ds_read_b128 v[198:201], v89 offset:29696
	s_waitcnt lgkmcnt(3)
	v_pk_fma_f32 v[76:77], v[52:53], v[202:203], v[76:77] op_sel_hi:[1,0,1]
	s_nop 0
	v_pk_fma_f32 v[72:73], v[42:43], v[202:203], v[76:77] op_sel:[0,1,0]
	s_nop 0
	v_pk_fma_f32 v[72:73], v[54:55], v[204:205], v[72:73] op_sel_hi:[1,0,1]
	v_mov_b32_e32 v204, v205
	v_pk_fma_f32 v[76:77], v[40:41], v[204:205], v[72:73] op_sel_hi:[1,0,1]
	ds_read_b128 v[202:205], v89 offset:30720
	s_waitcnt lgkmcnt(3)
	v_pk_fma_f32 v[76:77], v[56:57], v[206:207], v[76:77] op_sel_hi:[1,0,1]
	s_nop 0
	v_pk_fma_f32 v[72:73], v[8:9], v[206:207], v[76:77] op_sel:[0,1,0]
	s_nop 0
	v_pk_fma_f32 v[72:73], v[58:59], v[208:209], v[72:73] op_sel_hi:[1,0,1]
	v_mov_b32_e32 v208, v209
	v_pk_fma_f32 v[72:73], v[6:7], v[208:209], v[72:73] op_sel_hi:[1,0,1]
	ds_read_b128 v[206:209], v89 offset:31744
	s_waitcnt lgkmcnt(3)
	v_pk_fma_f32 v[78:79], v[44:45], v[194:195], 0 op_sel_hi:[1,0,0]
	s_nop 0
	v_pk_fma_f32 v[74:75], v[4:5], v[194:195], v[78:79] op_sel:[0,1,0]
	s_nop 0
	v_pk_fma_f32 v[74:75], v[46:47], v[196:197], v[74:75] op_sel_hi:[1,0,1]
	v_mov_b32_e32 v196, v197
	v_pk_fma_f32 v[78:79], v[2:3], v[196:197], v[74:75] op_sel_hi:[1,0,1]
	ds_read_b128 v[194:197], v89 offset:32768
	s_waitcnt lgkmcnt(3)
	v_pk_fma_f32 v[78:79], v[48:49], v[198:199], v[78:79] op_sel_hi:[1,0,1]
	s_nop 0
	v_pk_fma_f32 v[74:75], v[12:13], v[198:199], v[78:79] op_sel:[0,1,0]
	s_nop 0
	v_pk_fma_f32 v[74:75], v[50:51], v[200:201], v[74:75] op_sel_hi:[1,0,1]
	v_mov_b32_e32 v200, v201
	v_pk_fma_f32 v[78:79], v[10:11], v[200:201], v[74:75] op_sel_hi:[1,0,1]
	ds_read_b128 v[198:201], v89 offset:33792
	s_waitcnt lgkmcnt(3)
	v_pk_fma_f32 v[78:79], v[52:53], v[202:203], v[78:79] op_sel_hi:[1,0,1]
	s_nop 0
	v_pk_fma_f32 v[74:75], v[42:43], v[202:203], v[78:79] op_sel:[0,1,0]
	s_nop 0
	v_pk_fma_f32 v[74:75], v[54:55], v[204:205], v[74:75] op_sel_hi:[1,0,1]
	v_mov_b32_e32 v204, v205
	v_pk_fma_f32 v[78:79], v[40:41], v[204:205], v[74:75] op_sel_hi:[1,0,1]
	ds_read_b128 v[202:205], v89 offset:34816
	s_waitcnt lgkmcnt(3)
	v_pk_fma_f32 v[78:79], v[56:57], v[206:207], v[78:79] op_sel_hi:[1,0,1]
	s_nop 0
	v_pk_fma_f32 v[74:75], v[8:9], v[206:207], v[78:79] op_sel:[0,1,0]
	s_nop 0
	v_pk_fma_f32 v[74:75], v[58:59], v[208:209], v[74:75] op_sel_hi:[1,0,1]
	v_mov_b32_e32 v208, v209
	v_pk_fma_f32 v[74:75], v[6:7], v[208:209], v[74:75] op_sel_hi:[1,0,1]
	ds_read_b128 v[206:209], v89 offset:35840
	s_waitcnt lgkmcnt(3)
	v_pk_fma_f32 v[80:81], v[44:45], v[194:195], 0 op_sel_hi:[1,0,0]
	s_nop 0
	v_pk_fma_f32 v[76:77], v[4:5], v[194:195], v[80:81] op_sel:[0,1,0]
	s_nop 0
	v_pk_fma_f32 v[76:77], v[46:47], v[196:197], v[76:77] op_sel_hi:[1,0,1]
	v_mov_b32_e32 v196, v197
	v_pk_fma_f32 v[80:81], v[2:3], v[196:197], v[76:77] op_sel_hi:[1,0,1]
	ds_read_b128 v[194:197], v89 offset:36864
	s_waitcnt lgkmcnt(3)
	v_pk_fma_f32 v[80:81], v[48:49], v[198:199], v[80:81] op_sel_hi:[1,0,1]
	s_nop 0
	v_pk_fma_f32 v[76:77], v[12:13], v[198:199], v[80:81] op_sel:[0,1,0]
	s_nop 0
	v_pk_fma_f32 v[76:77], v[50:51], v[200:201], v[76:77] op_sel_hi:[1,0,1]
	v_mov_b32_e32 v200, v201
	v_pk_fma_f32 v[80:81], v[10:11], v[200:201], v[76:77] op_sel_hi:[1,0,1]
	ds_read_b128 v[198:201], v89 offset:37888
	s_waitcnt lgkmcnt(3)
	v_pk_fma_f32 v[80:81], v[52:53], v[202:203], v[80:81] op_sel_hi:[1,0,1]
	s_nop 0
	v_pk_fma_f32 v[76:77], v[42:43], v[202:203], v[80:81] op_sel:[0,1,0]
	s_nop 0
	v_pk_fma_f32 v[76:77], v[54:55], v[204:205], v[76:77] op_sel_hi:[1,0,1]
	v_mov_b32_e32 v204, v205
	v_pk_fma_f32 v[80:81], v[40:41], v[204:205], v[76:77] op_sel_hi:[1,0,1]
	ds_read_b128 v[202:205], v89 offset:38912
	s_waitcnt lgkmcnt(3)
	v_pk_fma_f32 v[80:81], v[56:57], v[206:207], v[80:81] op_sel_hi:[1,0,1]
	s_nop 0
	v_pk_fma_f32 v[76:77], v[8:9], v[206:207], v[80:81] op_sel:[0,1,0]
	s_nop 0
	v_pk_fma_f32 v[76:77], v[58:59], v[208:209], v[76:77] op_sel_hi:[1,0,1]
	v_mov_b32_e32 v208, v209
	v_pk_fma_f32 v[76:77], v[6:7], v[208:209], v[76:77] op_sel_hi:[1,0,1]
	ds_read_b128 v[206:209], v89 offset:39936
	s_nop 0
	v_permlane16_swap_b32_e32 v60, v76
	v_add_f32_e32 v60, v60, v76
	v_permlane16_swap_b32_e32 v61, v77
	s_waitcnt lgkmcnt(3)
	v_pk_fma_f32 v[82:83], v[44:45], v[194:195], 0 op_sel_hi:[1,0,0]
	s_nop 0
	v_pk_fma_f32 v[78:79], v[4:5], v[194:195], v[82:83] op_sel:[0,1,0]
	s_nop 0
	v_pk_fma_f32 v[78:79], v[46:47], v[196:197], v[78:79] op_sel_hi:[1,0,1]
	v_mov_b32_e32 v196, v197
	v_pk_fma_f32 v[82:83], v[2:3], v[196:197], v[78:79] op_sel_hi:[1,0,1]
	ds_read_b128 v[194:197], v89 offset:40960
	s_waitcnt lgkmcnt(3)
	v_pk_fma_f32 v[82:83], v[48:49], v[198:199], v[82:83] op_sel_hi:[1,0,1]
	s_nop 0
	v_pk_fma_f32 v[78:79], v[12:13], v[198:199], v[82:83] op_sel:[0,1,0]
	s_nop 0
	v_pk_fma_f32 v[78:79], v[50:51], v[200:201], v[78:79] op_sel_hi:[1,0,1]
	v_mov_b32_e32 v200, v201
	v_pk_fma_f32 v[82:83], v[10:11], v[200:201], v[78:79] op_sel_hi:[1,0,1]
	ds_read_b128 v[198:201], v89 offset:41984
	s_waitcnt lgkmcnt(3)
	v_pk_fma_f32 v[82:83], v[52:53], v[202:203], v[82:83] op_sel_hi:[1,0,1]
	s_nop 0
	v_pk_fma_f32 v[78:79], v[42:43], v[202:203], v[82:83] op_sel:[0,1,0]
	s_nop 0
	v_pk_fma_f32 v[78:79], v[54:55], v[204:205], v[78:79] op_sel_hi:[1,0,1]
	v_mov_b32_e32 v204, v205
	v_pk_fma_f32 v[82:83], v[40:41], v[204:205], v[78:79] op_sel_hi:[1,0,1]
	ds_read_b128 v[202:205], v89 offset:43008
	s_waitcnt lgkmcnt(3)
	v_pk_fma_f32 v[82:83], v[56:57], v[206:207], v[82:83] op_sel_hi:[1,0,1]
	s_nop 0
	v_pk_fma_f32 v[78:79], v[8:9], v[206:207], v[82:83] op_sel:[0,1,0]
	s_nop 0
	v_pk_fma_f32 v[78:79], v[58:59], v[208:209], v[78:79] op_sel_hi:[1,0,1]
	v_mov_b32_e32 v208, v209
	v_pk_fma_f32 v[78:79], v[6:7], v[208:209], v[78:79] op_sel_hi:[1,0,1]
	ds_read_b128 v[206:209], v89 offset:44032
	s_nop 0
	v_permlane16_swap_b32_e32 v62, v78
	v_add_f32_e32 v62, v62, v78
	v_permlane16_swap_b32_e32 v63, v79
	s_waitcnt lgkmcnt(3)
	v_pk_fma_f32 v[84:85], v[44:45], v[194:195], 0 op_sel_hi:[1,0,0]
	s_nop 0
	v_pk_fma_f32 v[80:81], v[4:5], v[194:195], v[84:85] op_sel:[0,1,0]
	s_nop 0
	v_pk_fma_f32 v[80:81], v[46:47], v[196:197], v[80:81] op_sel_hi:[1,0,1]
	v_mov_b32_e32 v196, v197
	v_pk_fma_f32 v[84:85], v[2:3], v[196:197], v[80:81] op_sel_hi:[1,0,1]
	ds_read_b128 v[194:197], v89 offset:45056
	s_waitcnt lgkmcnt(3)
	v_pk_fma_f32 v[84:85], v[48:49], v[198:199], v[84:85] op_sel_hi:[1,0,1]
	s_nop 0
	v_pk_fma_f32 v[80:81], v[12:13], v[198:199], v[84:85] op_sel:[0,1,0]
	s_nop 0
	v_pk_fma_f32 v[80:81], v[50:51], v[200:201], v[80:81] op_sel_hi:[1,0,1]
	v_mov_b32_e32 v200, v201
	v_pk_fma_f32 v[84:85], v[10:11], v[200:201], v[80:81] op_sel_hi:[1,0,1]
	ds_read_b128 v[198:201], v89 offset:46080
	s_waitcnt lgkmcnt(3)
	v_pk_fma_f32 v[84:85], v[52:53], v[202:203], v[84:85] op_sel_hi:[1,0,1]
	s_nop 0
	v_pk_fma_f32 v[80:81], v[42:43], v[202:203], v[84:85] op_sel:[0,1,0]
	s_nop 0
	v_pk_fma_f32 v[80:81], v[54:55], v[204:205], v[80:81] op_sel_hi:[1,0,1]
	v_mov_b32_e32 v204, v205
	v_pk_fma_f32 v[84:85], v[40:41], v[204:205], v[80:81] op_sel_hi:[1,0,1]
	ds_read_b128 v[202:205], v89 offset:47104
	s_waitcnt lgkmcnt(3)
	v_pk_fma_f32 v[84:85], v[56:57], v[206:207], v[84:85] op_sel_hi:[1,0,1]
	s_nop 0
	v_pk_fma_f32 v[80:81], v[8:9], v[206:207], v[84:85] op_sel:[0,1,0]
	s_nop 0
	v_pk_fma_f32 v[80:81], v[58:59], v[208:209], v[80:81] op_sel_hi:[1,0,1]
	v_mov_b32_e32 v208, v209
	v_pk_fma_f32 v[80:81], v[6:7], v[208:209], v[80:81] op_sel_hi:[1,0,1]
	ds_read_b128 v[206:209], v89 offset:48128
	s_nop 0
	v_permlane16_swap_b32_e32 v64, v80
	v_add_f32_e32 v64, v64, v80
	v_permlane16_swap_b32_e32 v65, v81
	s_waitcnt lgkmcnt(3)
	v_pk_fma_f32 v[86:87], v[44:45], v[194:195], 0 op_sel_hi:[1,0,0]
	s_nop 0
	v_pk_fma_f32 v[82:83], v[4:5], v[194:195], v[86:87] op_sel:[0,1,0]
	s_nop 0
	v_pk_fma_f32 v[82:83], v[46:47], v[196:197], v[82:83] op_sel_hi:[1,0,1]
	v_mov_b32_e32 v196, v197
	v_pk_fma_f32 v[86:87], v[2:3], v[196:197], v[82:83] op_sel_hi:[1,0,1]
	ds_read_b128 v[194:197], v89 offset:49152
	s_waitcnt lgkmcnt(3)
	v_pk_fma_f32 v[86:87], v[48:49], v[198:199], v[86:87] op_sel_hi:[1,0,1]
	s_nop 0
	v_pk_fma_f32 v[82:83], v[12:13], v[198:199], v[86:87] op_sel:[0,1,0]
	s_nop 0
	v_pk_fma_f32 v[82:83], v[50:51], v[200:201], v[82:83] op_sel_hi:[1,0,1]
	v_mov_b32_e32 v200, v201
	v_pk_fma_f32 v[86:87], v[10:11], v[200:201], v[82:83] op_sel_hi:[1,0,1]
	ds_read_b128 v[198:201], v89 offset:50176
	s_waitcnt lgkmcnt(3)
	v_pk_fma_f32 v[86:87], v[52:53], v[202:203], v[86:87] op_sel_hi:[1,0,1]
	s_nop 0
	v_pk_fma_f32 v[82:83], v[42:43], v[202:203], v[86:87] op_sel:[0,1,0]
	s_nop 0
	v_pk_fma_f32 v[82:83], v[54:55], v[204:205], v[82:83] op_sel_hi:[1,0,1]
	v_mov_b32_e32 v204, v205
	v_pk_fma_f32 v[86:87], v[40:41], v[204:205], v[82:83] op_sel_hi:[1,0,1]
	ds_read_b128 v[202:205], v89 offset:51200
	s_waitcnt lgkmcnt(3)
	v_pk_fma_f32 v[86:87], v[56:57], v[206:207], v[86:87] op_sel_hi:[1,0,1]
	s_nop 0
	v_pk_fma_f32 v[82:83], v[8:9], v[206:207], v[86:87] op_sel:[0,1,0]
	s_nop 0
	v_pk_fma_f32 v[82:83], v[58:59], v[208:209], v[82:83] op_sel_hi:[1,0,1]
	v_mov_b32_e32 v208, v209
	v_pk_fma_f32 v[82:83], v[6:7], v[208:209], v[82:83] op_sel_hi:[1,0,1]
	ds_read_b128 v[206:209], v89 offset:52224
	s_nop 0
	v_permlane16_swap_b32_e32 v66, v82
	v_add_f32_e32 v66, v66, v82
	v_permlane16_swap_b32_e32 v67, v83
	s_waitcnt lgkmcnt(3)
	v_pk_fma_f32 v[164:165], v[44:45], v[194:195], 0 op_sel_hi:[1,0,0]
	s_nop 0
	v_pk_fma_f32 v[84:85], v[4:5], v[194:195], v[164:165] op_sel:[0,1,0]
	s_nop 0
	v_pk_fma_f32 v[84:85], v[46:47], v[196:197], v[84:85] op_sel_hi:[1,0,1]
	v_mov_b32_e32 v196, v197
	v_pk_fma_f32 v[164:165], v[2:3], v[196:197], v[84:85] op_sel_hi:[1,0,1]
	ds_read_b128 v[194:197], v89 offset:53248
	s_waitcnt lgkmcnt(3)
	v_pk_fma_f32 v[164:165], v[48:49], v[198:199], v[164:165] op_sel_hi:[1,0,1]
	s_nop 0
	v_pk_fma_f32 v[84:85], v[12:13], v[198:199], v[164:165] op_sel:[0,1,0]
	s_nop 0
	v_pk_fma_f32 v[84:85], v[50:51], v[200:201], v[84:85] op_sel_hi:[1,0,1]
	v_mov_b32_e32 v200, v201
	v_pk_fma_f32 v[164:165], v[10:11], v[200:201], v[84:85] op_sel_hi:[1,0,1]
	ds_read_b128 v[198:201], v89 offset:54272
	s_waitcnt lgkmcnt(3)
	v_pk_fma_f32 v[164:165], v[52:53], v[202:203], v[164:165] op_sel_hi:[1,0,1]
	s_nop 0
	v_pk_fma_f32 v[84:85], v[42:43], v[202:203], v[164:165] op_sel:[0,1,0]
	s_nop 0
	v_pk_fma_f32 v[84:85], v[54:55], v[204:205], v[84:85] op_sel_hi:[1,0,1]
	v_mov_b32_e32 v204, v205
	v_pk_fma_f32 v[164:165], v[40:41], v[204:205], v[84:85] op_sel_hi:[1,0,1]
	ds_read_b128 v[202:205], v89 offset:55296
	s_waitcnt lgkmcnt(3)
	v_pk_fma_f32 v[164:165], v[56:57], v[206:207], v[164:165] op_sel_hi:[1,0,1]
	s_nop 0
	v_pk_fma_f32 v[84:85], v[8:9], v[206:207], v[164:165] op_sel:[0,1,0]
	v_pk_fma_f32 v[84:85], v[58:59], v[208:209], v[84:85] op_sel_hi:[1,0,1]
	v_mov_b32_e32 v208, v209
	v_pk_fma_f32 v[84:85], v[6:7], v[208:209], v[84:85] op_sel_hi:[1,0,1]
	ds_read_b128 v[206:209], v89 offset:56320
	s_waitcnt lgkmcnt(3)
	v_pk_fma_f32 v[86:87], v[44:45], v[194:195], 0 op_sel_hi:[1,0,0]
	s_nop 0
	v_pk_fma_f32 v[86:87], v[4:5], v[194:195], v[86:87] op_sel:[0,1,0]
	v_mov_b32_e32 v194, v197
	v_pk_fma_f32 v[86:87], v[46:47], v[196:197], v[86:87] op_sel_hi:[1,0,1]
	v_permlane16_swap_b32_e32 v68, v84
	v_pk_fma_f32 v[86:87], v[2:3], v[194:195], v[86:87] op_sel_hi:[1,0,1]
	ds_read_b128 v[194:197], v89 offset:57344
	v_add_f32_e32 v68, v68, v84
	v_cndmask_b32_e64 v76, v60, v68, s[40:41]
	v_cndmask_b32_e64 v60, v68, v60, s[40:41]
	v_permlane16_swap_b32_e32 v69, v85
	s_waitcnt lgkmcnt(3)
	v_pk_fma_f32 v[86:87], v[48:49], v[198:199], v[86:87] op_sel_hi:[1,0,1]
	v_add_f32_dpp v60, v76, v60 row_mirror row_mask:0xf bank_mask:0xf bound_ctrl:1
	v_pk_fma_f32 v[86:87], v[12:13], v[198:199], v[86:87] op_sel:[0,1,0]
	v_mov_b32_e32 v198, v201
	v_pk_fma_f32 v[86:87], v[50:51], v[200:201], v[86:87] op_sel_hi:[1,0,1]
	s_nop 0
	v_pk_fma_f32 v[86:87], v[10:11], v[198:199], v[86:87] op_sel_hi:[1,0,1]
	ds_read_b128 v[198:201], v89 offset:58368
	s_waitcnt lgkmcnt(3)
	v_pk_fma_f32 v[86:87], v[52:53], v[202:203], v[86:87] op_sel_hi:[1,0,1]
	s_nop 0
	v_pk_fma_f32 v[86:87], v[42:43], v[202:203], v[86:87] op_sel:[0,1,0]
	v_mov_b32_e32 v202, v205
	v_pk_fma_f32 v[86:87], v[54:55], v[204:205], v[86:87] op_sel_hi:[1,0,1]
	s_nop 0
	v_pk_fma_f32 v[86:87], v[40:41], v[202:203], v[86:87] op_sel_hi:[1,0,1]
	ds_read_b128 v[202:205], v89 offset:59392
	s_waitcnt lgkmcnt(3)
	v_pk_fma_f32 v[86:87], v[56:57], v[206:207], v[86:87] op_sel_hi:[1,0,1]
	s_nop 0
	v_pk_fma_f32 v[86:87], v[8:9], v[206:207], v[86:87] op_sel:[0,1,0]
	v_mov_b32_e32 v206, v209
	v_pk_fma_f32 v[86:87], v[58:59], v[208:209], v[86:87] op_sel_hi:[1,0,1]
	s_nop 0
	v_pk_fma_f32 v[86:87], v[6:7], v[206:207], v[86:87] op_sel_hi:[1,0,1]
	ds_read_b128 v[206:209], v89 offset:60416
	s_nop 0
	v_permlane16_swap_b32_e32 v70, v86
	v_add_f32_e32 v70, v70, v86
	v_cndmask_b32_e64 v68, v62, v70, s[40:41]
	s_waitcnt lgkmcnt(3)
	v_pk_fma_f32 v[168:169], v[44:45], v[194:195], 0 op_sel_hi:[1,0,0]
	v_cndmask_b32_e64 v62, v70, v62, s[40:41]
	v_pk_fma_f32 v[164:165], v[4:5], v[194:195], v[168:169] op_sel:[0,1,0]
	v_permlane16_swap_b32_e32 v71, v87
	v_pk_fma_f32 v[164:165], v[46:47], v[196:197], v[164:165] op_sel_hi:[1,0,1]
	v_mov_b32_e32 v196, v197
	v_pk_fma_f32 v[168:169], v[2:3], v[196:197], v[164:165] op_sel_hi:[1,0,1]
	ds_read_b128 v[194:197], v89 offset:61440
	v_add_f32_dpp v62, v68, v62 row_mirror row_mask:0xf bank_mask:0xf bound_ctrl:1
	s_waitcnt lgkmcnt(3)
	v_pk_fma_f32 v[168:169], v[48:49], v[198:199], v[168:169] op_sel_hi:[1,0,1]
	s_nop 0
	v_pk_fma_f32 v[164:165], v[12:13], v[198:199], v[168:169] op_sel:[0,1,0]
	s_nop 0
	v_pk_fma_f32 v[164:165], v[50:51], v[200:201], v[164:165] op_sel_hi:[1,0,1]
	v_mov_b32_e32 v200, v201
	v_pk_fma_f32 v[168:169], v[10:11], v[200:201], v[164:165] op_sel_hi:[1,0,1]
	ds_read_b128 v[198:201], v89 offset:62464
	s_waitcnt lgkmcnt(3)
	v_pk_fma_f32 v[168:169], v[52:53], v[202:203], v[168:169] op_sel_hi:[1,0,1]
	s_nop 0
	v_pk_fma_f32 v[164:165], v[42:43], v[202:203], v[168:169] op_sel:[0,1,0]
	s_nop 0
	v_pk_fma_f32 v[164:165], v[54:55], v[204:205], v[164:165] op_sel_hi:[1,0,1]
	v_mov_b32_e32 v204, v205
	v_pk_fma_f32 v[168:169], v[40:41], v[204:205], v[164:165] op_sel_hi:[1,0,1]
	ds_read_b128 v[202:205], v89 offset:63488
	s_waitcnt lgkmcnt(3)
	v_pk_fma_f32 v[168:169], v[56:57], v[206:207], v[168:169] op_sel_hi:[1,0,1]
	s_nop 0
	v_pk_fma_f32 v[164:165], v[8:9], v[206:207], v[168:169] op_sel:[0,1,0]
	s_nop 0
	v_pk_fma_f32 v[164:165], v[58:59], v[208:209], v[164:165] op_sel_hi:[1,0,1]
	v_mov_b32_e32 v208, v209
	v_pk_fma_f32 v[168:169], v[6:7], v[208:209], v[164:165] op_sel_hi:[1,0,1]
	ds_read_b128 v[206:209], v89 offset:64512
	s_nop 0
	v_permlane16_swap_b32_e32 v72, v168
	v_add_f32_e32 v72, v72, v168
	v_cndmask_b32_e64 v68, v64, v72, s[40:41]
	s_waitcnt lgkmcnt(3)
	v_pk_fma_f32 v[170:171], v[44:45], v[194:195], 0 op_sel_hi:[1,0,0]
	v_cndmask_b32_e64 v64, v72, v64, s[40:41]
	v_pk_fma_f32 v[164:165], v[4:5], v[194:195], v[170:171] op_sel:[0,1,0]
	v_permlane16_swap_b32_e32 v73, v169
	v_pk_fma_f32 v[164:165], v[46:47], v[196:197], v[164:165] op_sel_hi:[1,0,1]
	v_mov_b32_e32 v196, v197
	v_pk_fma_f32 v[170:171], v[2:3], v[196:197], v[164:165] op_sel_hi:[1,0,1]
	ds_read_b128 v[194:197], v90
	v_add_f32_dpp v64, v68, v64 row_mirror row_mask:0xf bank_mask:0xf bound_ctrl:1
	s_waitcnt lgkmcnt(3)
	v_pk_fma_f32 v[170:171], v[48:49], v[198:199], v[170:171] op_sel_hi:[1,0,1]
	s_nop 0
	v_pk_fma_f32 v[164:165], v[12:13], v[198:199], v[170:171] op_sel:[0,1,0]
	s_nop 0
	v_pk_fma_f32 v[164:165], v[50:51], v[200:201], v[164:165] op_sel_hi:[1,0,1]
	v_mov_b32_e32 v200, v201
	v_pk_fma_f32 v[170:171], v[10:11], v[200:201], v[164:165] op_sel_hi:[1,0,1]
	ds_read_b128 v[198:201], v91
	s_waitcnt lgkmcnt(3)
	v_pk_fma_f32 v[170:171], v[52:53], v[202:203], v[170:171] op_sel_hi:[1,0,1]
	s_nop 0
	v_pk_fma_f32 v[164:165], v[42:43], v[202:203], v[170:171] op_sel:[0,1,0]
	s_nop 0
	v_pk_fma_f32 v[164:165], v[54:55], v[204:205], v[164:165] op_sel_hi:[1,0,1]
	v_mov_b32_e32 v204, v205
	v_pk_fma_f32 v[170:171], v[40:41], v[204:205], v[164:165] op_sel_hi:[1,0,1]
	ds_read_b128 v[202:205], v92
	s_waitcnt lgkmcnt(3)
	v_pk_fma_f32 v[170:171], v[56:57], v[206:207], v[170:171] op_sel_hi:[1,0,1]
	s_nop 0
	v_pk_fma_f32 v[164:165], v[8:9], v[206:207], v[170:171] op_sel:[0,1,0]
	s_nop 0
	v_pk_fma_f32 v[164:165], v[58:59], v[208:209], v[164:165] op_sel_hi:[1,0,1]
	v_mov_b32_e32 v208, v209
	v_pk_fma_f32 v[164:165], v[6:7], v[208:209], v[164:165] op_sel_hi:[1,0,1]
	s_nop 1
	v_permlane16_swap_b32_e32 v74, v164
	v_add_f32_e32 v74, v74, v164
	v_cndmask_b32_e64 v68, v66, v74, s[40:41]
	v_cndmask_b32_e64 v66, v74, v66, s[40:41]
	v_permlane16_swap_b32_e32 v75, v165
	s_nop 0
	v_add_f32_dpp v66, v68, v66 row_mirror row_mask:0xf bank_mask:0xf bound_ctrl:1
	v_cndmask_b32_e64 v68, v60, v64, s[42:43]
	v_cndmask_b32_e64 v60, v64, v60, s[42:43]
	v_cndmask_b32_e64 v64, v62, v66, s[42:43]
	v_cndmask_b32_e64 v62, v66, v62, s[42:43]
	v_add_f32_dpp v60, v68, v60 row_half_mirror row_mask:0xf bank_mask:0xf bound_ctrl:1
	v_add_f32_e32 v66, v73, v169
	v_add_f32_dpp v62, v64, v62 row_half_mirror row_mask:0xf bank_mask:0xf bound_ctrl:1
	v_cndmask_b32_e64 v64, v60, v62, s[44:45]
	v_cndmask_b32_e64 v60, v62, v60, s[44:45]
	s_nop 1
	v_add_f32_dpp v60, v64, v60 quad_perm:[2,3,0,1] row_mask:0xf bank_mask:0xf bound_ctrl:1
	v_add_f32_e32 v64, v69, v85
	s_nop 0
	v_add_f32_dpp v60, v60, v60 quad_perm:[1,0,3,2] row_mask:0xf bank_mask:0xf bound_ctrl:1
	v_mov_b32_e32 v62, v60
	s_nop 1
	v_permlane32_swap_b32_e32 v60, v62
	v_add_f32_e32 v60, v60, v62
	v_cndmask_b32_e64 v166, 0, v60, s[46:47]
	v_add_f32_e32 v60, v61, v77
	v_add_f32_e32 v61, v63, v79
	v_add_f32_e32 v62, v65, v81
	v_add_f32_e32 v65, v71, v87
	v_cndmask_b32_e64 v68, v60, v64, s[40:41]
	v_cndmask_b32_e64 v60, v64, v60, s[40:41]
	v_cndmask_b32_e64 v64, v61, v65, s[40:41]
	v_cndmask_b32_e64 v61, v65, v61, s[40:41]
	v_add_f32_e32 v63, v67, v83
	v_add_f32_e32 v67, v75, v165
	v_add_f32_dpp v61, v64, v61 row_mirror row_mask:0xf bank_mask:0xf bound_ctrl:1
	v_cndmask_b32_e64 v64, v62, v66, s[40:41]
	v_cndmask_b32_e64 v62, v66, v62, s[40:41]
	v_add_f32_dpp v60, v68, v60 row_mirror row_mask:0xf bank_mask:0xf bound_ctrl:1
	s_nop 0
	v_add_f32_dpp v62, v64, v62 row_mirror row_mask:0xf bank_mask:0xf bound_ctrl:1
	v_cndmask_b32_e64 v64, v63, v67, s[40:41]
	v_cndmask_b32_e64 v63, v67, v63, s[40:41]
	s_nop 1
	v_add_f32_dpp v63, v64, v63 row_mirror row_mask:0xf bank_mask:0xf bound_ctrl:1
	v_cndmask_b32_e64 v64, v60, v62, s[42:43]
	v_cndmask_b32_e64 v60, v62, v60, s[42:43]
	v_cndmask_b32_e64 v62, v61, v63, s[42:43]
	v_cndmask_b32_e64 v61, v63, v61, s[42:43]
	v_add_f32_dpp v60, v64, v60 row_half_mirror row_mask:0xf bank_mask:0xf bound_ctrl:1
	s_nop 0
	v_add_f32_dpp v61, v62, v61 row_half_mirror row_mask:0xf bank_mask:0xf bound_ctrl:1
	v_cndmask_b32_e64 v62, v60, v61, s[44:45]
	v_cndmask_b32_e64 v60, v61, v60, s[44:45]
	s_nop 1
	v_add_f32_dpp v60, v62, v60 quad_perm:[2,3,0,1] row_mask:0xf bank_mask:0xf bound_ctrl:1
	s_nop 1
	v_add_f32_dpp v164, v60, v60 quad_perm:[1,0,3,2] row_mask:0xf bank_mask:0xf bound_ctrl:1
	ds_read_b128 v[206:209], v93
	v_mov_b32_e32 v165, v164
	s_nop 1
	v_permlane32_swap_b32_e32 v164, v165
	s_waitcnt lgkmcnt(3)
	v_pk_fma_f32 v[64:65], v[44:45], v[194:195], 0 op_sel_hi:[1,0,0]
	s_nop 0
	v_pk_fma_f32 v[60:61], v[4:5], v[194:195], v[64:65] op_sel:[0,1,0]
	s_nop 0
	v_pk_fma_f32 v[60:61], v[46:47], v[196:197], v[60:61] op_sel_hi:[1,0,1]
	v_mov_b32_e32 v196, v197
	v_pk_fma_f32 v[64:65], v[2:3], v[196:197], v[60:61] op_sel_hi:[1,0,1]
	ds_read_b128 v[194:197], v94
	s_waitcnt lgkmcnt(3)
	v_pk_fma_f32 v[64:65], v[48:49], v[198:199], v[64:65] op_sel_hi:[1,0,1]
	s_nop 0
	v_pk_fma_f32 v[60:61], v[12:13], v[198:199], v[64:65] op_sel:[0,1,0]
	s_nop 0
	v_pk_fma_f32 v[60:61], v[50:51], v[200:201], v[60:61] op_sel_hi:[1,0,1]
	v_mov_b32_e32 v200, v201
	v_pk_fma_f32 v[64:65], v[10:11], v[200:201], v[60:61] op_sel_hi:[1,0,1]
	ds_read_b128 v[198:201], v95
	s_waitcnt lgkmcnt(3)
	v_pk_fma_f32 v[64:65], v[52:53], v[202:203], v[64:65] op_sel_hi:[1,0,1]
	s_nop 0
	v_pk_fma_f32 v[60:61], v[42:43], v[202:203], v[64:65] op_sel:[0,1,0]
	s_nop 0
	v_pk_fma_f32 v[60:61], v[54:55], v[204:205], v[60:61] op_sel_hi:[1,0,1]
	v_mov_b32_e32 v204, v205
	v_pk_fma_f32 v[64:65], v[40:41], v[204:205], v[60:61] op_sel_hi:[1,0,1]
	ds_read_b128 v[202:205], v96
	s_waitcnt lgkmcnt(3)
	v_pk_fma_f32 v[64:65], v[56:57], v[206:207], v[64:65] op_sel_hi:[1,0,1]
	s_nop 0
	v_pk_fma_f32 v[60:61], v[8:9], v[206:207], v[64:65] op_sel:[0,1,0]
	s_nop 0
	v_pk_fma_f32 v[60:61], v[58:59], v[208:209], v[60:61] op_sel_hi:[1,0,1]
	v_mov_b32_e32 v208, v209
	v_pk_fma_f32 v[60:61], v[6:7], v[208:209], v[60:61] op_sel_hi:[1,0,1]
	ds_read_b128 v[206:209], v97
	s_waitcnt lgkmcnt(3)
	v_pk_fma_f32 v[66:67], v[44:45], v[194:195], 0 op_sel_hi:[1,0,0]
	s_nop 0
	v_pk_fma_f32 v[62:63], v[4:5], v[194:195], v[66:67] op_sel:[0,1,0]
	s_nop 0
	v_pk_fma_f32 v[62:63], v[46:47], v[196:197], v[62:63] op_sel_hi:[1,0,1]
	v_mov_b32_e32 v196, v197
	v_pk_fma_f32 v[66:67], v[2:3], v[196:197], v[62:63] op_sel_hi:[1,0,1]
	ds_read_b128 v[194:197], v98
	s_waitcnt lgkmcnt(3)
	v_pk_fma_f32 v[66:67], v[48:49], v[198:199], v[66:67] op_sel_hi:[1,0,1]
	s_nop 0
	v_pk_fma_f32 v[62:63], v[12:13], v[198:199], v[66:67] op_sel:[0,1,0]
	s_nop 0
	v_pk_fma_f32 v[62:63], v[50:51], v[200:201], v[62:63] op_sel_hi:[1,0,1]
	v_mov_b32_e32 v200, v201
	v_pk_fma_f32 v[66:67], v[10:11], v[200:201], v[62:63] op_sel_hi:[1,0,1]
	ds_read_b128 v[198:201], v99
	s_waitcnt lgkmcnt(3)
	v_pk_fma_f32 v[66:67], v[52:53], v[202:203], v[66:67] op_sel_hi:[1,0,1]
	s_nop 0
	v_pk_fma_f32 v[62:63], v[42:43], v[202:203], v[66:67] op_sel:[0,1,0]
	s_nop 0
	v_pk_fma_f32 v[62:63], v[54:55], v[204:205], v[62:63] op_sel_hi:[1,0,1]
	v_mov_b32_e32 v204, v205
	v_pk_fma_f32 v[66:67], v[40:41], v[204:205], v[62:63] op_sel_hi:[1,0,1]
	ds_read_b128 v[202:205], v100
	s_waitcnt lgkmcnt(3)
	v_pk_fma_f32 v[66:67], v[56:57], v[206:207], v[66:67] op_sel_hi:[1,0,1]
	s_nop 0
	v_pk_fma_f32 v[62:63], v[8:9], v[206:207], v[66:67] op_sel:[0,1,0]
	s_nop 0
	v_pk_fma_f32 v[62:63], v[58:59], v[208:209], v[62:63] op_sel_hi:[1,0,1]
	v_mov_b32_e32 v208, v209
	v_pk_fma_f32 v[62:63], v[6:7], v[208:209], v[62:63] op_sel_hi:[1,0,1]
	ds_read_b128 v[206:209], v102
	s_waitcnt lgkmcnt(3)
	v_pk_fma_f32 v[68:69], v[44:45], v[194:195], 0 op_sel_hi:[1,0,0]
	s_nop 0
	v_pk_fma_f32 v[64:65], v[4:5], v[194:195], v[68:69] op_sel:[0,1,0]
	s_nop 0
	v_pk_fma_f32 v[64:65], v[46:47], v[196:197], v[64:65] op_sel_hi:[1,0,1]
	v_mov_b32_e32 v196, v197
	v_pk_fma_f32 v[68:69], v[2:3], v[196:197], v[64:65] op_sel_hi:[1,0,1]
	ds_read_b128 v[194:197], v103
	s_waitcnt lgkmcnt(3)
	v_pk_fma_f32 v[68:69], v[48:49], v[198:199], v[68:69] op_sel_hi:[1,0,1]
	s_nop 0
	v_pk_fma_f32 v[64:65], v[12:13], v[198:199], v[68:69] op_sel:[0,1,0]
	s_nop 0
	v_pk_fma_f32 v[64:65], v[50:51], v[200:201], v[64:65] op_sel_hi:[1,0,1]
	v_mov_b32_e32 v200, v201
	v_pk_fma_f32 v[68:69], v[10:11], v[200:201], v[64:65] op_sel_hi:[1,0,1]
	ds_read_b128 v[198:201], v104
	s_waitcnt lgkmcnt(3)
	v_pk_fma_f32 v[68:69], v[52:53], v[202:203], v[68:69] op_sel_hi:[1,0,1]
	s_nop 0
	v_pk_fma_f32 v[64:65], v[42:43], v[202:203], v[68:69] op_sel:[0,1,0]
	s_nop 0
	v_pk_fma_f32 v[64:65], v[54:55], v[204:205], v[64:65] op_sel_hi:[1,0,1]
	v_mov_b32_e32 v204, v205
	v_pk_fma_f32 v[68:69], v[40:41], v[204:205], v[64:65] op_sel_hi:[1,0,1]
	ds_read_b128 v[202:205], v105
	s_waitcnt lgkmcnt(3)
	v_pk_fma_f32 v[68:69], v[56:57], v[206:207], v[68:69] op_sel_hi:[1,0,1]
	s_nop 0
	v_pk_fma_f32 v[64:65], v[8:9], v[206:207], v[68:69] op_sel:[0,1,0]
	s_nop 0
	v_pk_fma_f32 v[64:65], v[58:59], v[208:209], v[64:65] op_sel_hi:[1,0,1]
	v_mov_b32_e32 v208, v209
	v_pk_fma_f32 v[64:65], v[6:7], v[208:209], v[64:65] op_sel_hi:[1,0,1]
	ds_read_b128 v[206:209], v106
	s_waitcnt lgkmcnt(3)
	v_pk_fma_f32 v[70:71], v[44:45], v[194:195], 0 op_sel_hi:[1,0,0]
	s_nop 0
	v_pk_fma_f32 v[66:67], v[4:5], v[194:195], v[70:71] op_sel:[0,1,0]
	s_nop 0
	v_pk_fma_f32 v[66:67], v[46:47], v[196:197], v[66:67] op_sel_hi:[1,0,1]
	v_mov_b32_e32 v196, v197
	v_pk_fma_f32 v[70:71], v[2:3], v[196:197], v[66:67] op_sel_hi:[1,0,1]
	ds_read_b128 v[194:197], v107
	s_waitcnt lgkmcnt(3)
	v_pk_fma_f32 v[70:71], v[48:49], v[198:199], v[70:71] op_sel_hi:[1,0,1]
	s_nop 0
	v_pk_fma_f32 v[66:67], v[12:13], v[198:199], v[70:71] op_sel:[0,1,0]
	s_nop 0
	v_pk_fma_f32 v[66:67], v[50:51], v[200:201], v[66:67] op_sel_hi:[1,0,1]
	v_mov_b32_e32 v200, v201
	v_pk_fma_f32 v[70:71], v[10:11], v[200:201], v[66:67] op_sel_hi:[1,0,1]
	ds_read_b128 v[198:201], v108
	s_waitcnt lgkmcnt(3)
	v_pk_fma_f32 v[70:71], v[52:53], v[202:203], v[70:71] op_sel_hi:[1,0,1]
	s_nop 0
	v_pk_fma_f32 v[66:67], v[42:43], v[202:203], v[70:71] op_sel:[0,1,0]
	s_nop 0
	v_pk_fma_f32 v[66:67], v[54:55], v[204:205], v[66:67] op_sel_hi:[1,0,1]
	v_mov_b32_e32 v204, v205
	v_pk_fma_f32 v[70:71], v[40:41], v[204:205], v[66:67] op_sel_hi:[1,0,1]
	ds_read_b128 v[202:205], v109
	s_waitcnt lgkmcnt(3)
	v_pk_fma_f32 v[70:71], v[56:57], v[206:207], v[70:71] op_sel_hi:[1,0,1]
	s_nop 0
	v_pk_fma_f32 v[66:67], v[8:9], v[206:207], v[70:71] op_sel:[0,1,0]
	s_nop 0
	v_pk_fma_f32 v[66:67], v[58:59], v[208:209], v[66:67] op_sel_hi:[1,0,1]
	v_mov_b32_e32 v208, v209
	v_pk_fma_f32 v[66:67], v[6:7], v[208:209], v[66:67] op_sel_hi:[1,0,1]
	ds_read_b128 v[206:209], v110
	s_waitcnt lgkmcnt(3)
	v_pk_fma_f32 v[72:73], v[44:45], v[194:195], 0 op_sel_hi:[1,0,0]
	s_nop 0
	v_pk_fma_f32 v[68:69], v[4:5], v[194:195], v[72:73] op_sel:[0,1,0]
	s_nop 0
	v_pk_fma_f32 v[68:69], v[46:47], v[196:197], v[68:69] op_sel_hi:[1,0,1]
	v_mov_b32_e32 v196, v197
	v_pk_fma_f32 v[72:73], v[2:3], v[196:197], v[68:69] op_sel_hi:[1,0,1]
	ds_read_b128 v[194:197], v111
	s_waitcnt lgkmcnt(3)
	v_pk_fma_f32 v[72:73], v[48:49], v[198:199], v[72:73] op_sel_hi:[1,0,1]
	s_nop 0
	v_pk_fma_f32 v[68:69], v[12:13], v[198:199], v[72:73] op_sel:[0,1,0]
	s_nop 0
	v_pk_fma_f32 v[68:69], v[50:51], v[200:201], v[68:69] op_sel_hi:[1,0,1]
	v_mov_b32_e32 v200, v201
	v_pk_fma_f32 v[72:73], v[10:11], v[200:201], v[68:69] op_sel_hi:[1,0,1]
	ds_read_b128 v[198:201], v112
	s_waitcnt lgkmcnt(3)
	v_pk_fma_f32 v[72:73], v[52:53], v[202:203], v[72:73] op_sel_hi:[1,0,1]
	s_nop 0
	v_pk_fma_f32 v[68:69], v[42:43], v[202:203], v[72:73] op_sel:[0,1,0]
	s_nop 0
	v_pk_fma_f32 v[68:69], v[54:55], v[204:205], v[68:69] op_sel_hi:[1,0,1]
	v_mov_b32_e32 v204, v205
	v_pk_fma_f32 v[72:73], v[40:41], v[204:205], v[68:69] op_sel_hi:[1,0,1]
	ds_read_b128 v[202:205], v113
	s_waitcnt lgkmcnt(3)
	v_pk_fma_f32 v[72:73], v[56:57], v[206:207], v[72:73] op_sel_hi:[1,0,1]
	s_nop 0
	v_pk_fma_f32 v[68:69], v[8:9], v[206:207], v[72:73] op_sel:[0,1,0]
	s_nop 0
	v_pk_fma_f32 v[68:69], v[58:59], v[208:209], v[68:69] op_sel_hi:[1,0,1]
	v_mov_b32_e32 v208, v209
	v_pk_fma_f32 v[68:69], v[6:7], v[208:209], v[68:69] op_sel_hi:[1,0,1]
	ds_read_b128 v[206:209], v114
	s_waitcnt lgkmcnt(3)
	v_pk_fma_f32 v[74:75], v[44:45], v[194:195], 0 op_sel_hi:[1,0,0]
	s_nop 0
	v_pk_fma_f32 v[70:71], v[4:5], v[194:195], v[74:75] op_sel:[0,1,0]
	s_nop 0
	v_pk_fma_f32 v[70:71], v[46:47], v[196:197], v[70:71] op_sel_hi:[1,0,1]
	v_mov_b32_e32 v196, v197
	v_pk_fma_f32 v[74:75], v[2:3], v[196:197], v[70:71] op_sel_hi:[1,0,1]
	ds_read_b128 v[194:197], v115
	s_waitcnt lgkmcnt(3)
	v_pk_fma_f32 v[74:75], v[48:49], v[198:199], v[74:75] op_sel_hi:[1,0,1]
	s_nop 0
	v_pk_fma_f32 v[70:71], v[12:13], v[198:199], v[74:75] op_sel:[0,1,0]
	s_nop 0
	v_pk_fma_f32 v[70:71], v[50:51], v[200:201], v[70:71] op_sel_hi:[1,0,1]
	v_mov_b32_e32 v200, v201
	v_pk_fma_f32 v[74:75], v[10:11], v[200:201], v[70:71] op_sel_hi:[1,0,1]
	ds_read_b128 v[198:201], v116
	s_waitcnt lgkmcnt(3)
	v_pk_fma_f32 v[74:75], v[52:53], v[202:203], v[74:75] op_sel_hi:[1,0,1]
	s_nop 0
	v_pk_fma_f32 v[70:71], v[42:43], v[202:203], v[74:75] op_sel:[0,1,0]
	s_nop 0
	v_pk_fma_f32 v[70:71], v[54:55], v[204:205], v[70:71] op_sel_hi:[1,0,1]
	v_mov_b32_e32 v204, v205
	v_pk_fma_f32 v[74:75], v[40:41], v[204:205], v[70:71] op_sel_hi:[1,0,1]
	ds_read_b128 v[202:205], v117
	s_waitcnt lgkmcnt(3)
	v_pk_fma_f32 v[74:75], v[56:57], v[206:207], v[74:75] op_sel_hi:[1,0,1]
	s_nop 0
	v_pk_fma_f32 v[70:71], v[8:9], v[206:207], v[74:75] op_sel:[0,1,0]
	s_nop 0
	v_pk_fma_f32 v[70:71], v[58:59], v[208:209], v[70:71] op_sel_hi:[1,0,1]
	v_mov_b32_e32 v208, v209
	v_pk_fma_f32 v[70:71], v[6:7], v[208:209], v[70:71] op_sel_hi:[1,0,1]
	ds_read_b128 v[206:209], v118
	s_waitcnt lgkmcnt(3)
	v_pk_fma_f32 v[76:77], v[44:45], v[194:195], 0 op_sel_hi:[1,0,0]
	s_nop 0
	v_pk_fma_f32 v[72:73], v[4:5], v[194:195], v[76:77] op_sel:[0,1,0]
	s_nop 0
	v_pk_fma_f32 v[72:73], v[46:47], v[196:197], v[72:73] op_sel_hi:[1,0,1]
	v_mov_b32_e32 v196, v197
	v_pk_fma_f32 v[76:77], v[2:3], v[196:197], v[72:73] op_sel_hi:[1,0,1]
	ds_read_b128 v[194:197], v119
	s_waitcnt lgkmcnt(3)
	v_pk_fma_f32 v[76:77], v[48:49], v[198:199], v[76:77] op_sel_hi:[1,0,1]
	s_nop 0
	v_pk_fma_f32 v[72:73], v[12:13], v[198:199], v[76:77] op_sel:[0,1,0]
	s_nop 0
	v_pk_fma_f32 v[72:73], v[50:51], v[200:201], v[72:73] op_sel_hi:[1,0,1]
	v_mov_b32_e32 v200, v201
	v_pk_fma_f32 v[76:77], v[10:11], v[200:201], v[72:73] op_sel_hi:[1,0,1]
	ds_read_b128 v[198:201], v120
	s_waitcnt lgkmcnt(3)
	v_pk_fma_f32 v[76:77], v[52:53], v[202:203], v[76:77] op_sel_hi:[1,0,1]
	s_nop 0
	v_pk_fma_f32 v[72:73], v[42:43], v[202:203], v[76:77] op_sel:[0,1,0]
	s_nop 0
	v_pk_fma_f32 v[72:73], v[54:55], v[204:205], v[72:73] op_sel_hi:[1,0,1]
	v_mov_b32_e32 v204, v205
	v_pk_fma_f32 v[76:77], v[40:41], v[204:205], v[72:73] op_sel_hi:[1,0,1]
	ds_read_b128 v[202:205], v121
	s_waitcnt lgkmcnt(3)
	v_pk_fma_f32 v[76:77], v[56:57], v[206:207], v[76:77] op_sel_hi:[1,0,1]
	s_nop 0
	v_pk_fma_f32 v[72:73], v[8:9], v[206:207], v[76:77] op_sel:[0,1,0]
	s_nop 0
	v_pk_fma_f32 v[72:73], v[58:59], v[208:209], v[72:73] op_sel_hi:[1,0,1]
	v_mov_b32_e32 v208, v209
	v_pk_fma_f32 v[72:73], v[6:7], v[208:209], v[72:73] op_sel_hi:[1,0,1]
	ds_read_b128 v[206:209], v122
	s_waitcnt lgkmcnt(3)
	v_pk_fma_f32 v[78:79], v[44:45], v[194:195], 0 op_sel_hi:[1,0,0]
	s_nop 0
	v_pk_fma_f32 v[74:75], v[4:5], v[194:195], v[78:79] op_sel:[0,1,0]
	s_nop 0
	v_pk_fma_f32 v[74:75], v[46:47], v[196:197], v[74:75] op_sel_hi:[1,0,1]
	v_mov_b32_e32 v196, v197
	v_pk_fma_f32 v[78:79], v[2:3], v[196:197], v[74:75] op_sel_hi:[1,0,1]
	ds_read_b128 v[194:197], v123
	s_waitcnt lgkmcnt(3)
	v_pk_fma_f32 v[78:79], v[48:49], v[198:199], v[78:79] op_sel_hi:[1,0,1]
	s_nop 0
	v_pk_fma_f32 v[74:75], v[12:13], v[198:199], v[78:79] op_sel:[0,1,0]
	s_nop 0
	v_pk_fma_f32 v[74:75], v[50:51], v[200:201], v[74:75] op_sel_hi:[1,0,1]
	v_mov_b32_e32 v200, v201
	v_pk_fma_f32 v[78:79], v[10:11], v[200:201], v[74:75] op_sel_hi:[1,0,1]
	ds_read_b128 v[198:201], v124
	s_waitcnt lgkmcnt(3)
	v_pk_fma_f32 v[78:79], v[52:53], v[202:203], v[78:79] op_sel_hi:[1,0,1]
	s_nop 0
	v_pk_fma_f32 v[74:75], v[42:43], v[202:203], v[78:79] op_sel:[0,1,0]
	s_nop 0
	v_pk_fma_f32 v[74:75], v[54:55], v[204:205], v[74:75] op_sel_hi:[1,0,1]
	v_mov_b32_e32 v204, v205
	v_pk_fma_f32 v[78:79], v[40:41], v[204:205], v[74:75] op_sel_hi:[1,0,1]
	ds_read_b128 v[202:205], v125
	s_waitcnt lgkmcnt(3)
	v_pk_fma_f32 v[78:79], v[56:57], v[206:207], v[78:79] op_sel_hi:[1,0,1]
	s_nop 0
	v_pk_fma_f32 v[74:75], v[8:9], v[206:207], v[78:79] op_sel:[0,1,0]
	s_nop 0
	v_pk_fma_f32 v[74:75], v[58:59], v[208:209], v[74:75] op_sel_hi:[1,0,1]
	v_mov_b32_e32 v208, v209
	v_pk_fma_f32 v[74:75], v[6:7], v[208:209], v[74:75] op_sel_hi:[1,0,1]
	ds_read_b128 v[206:209], v126
	s_waitcnt lgkmcnt(3)
	v_pk_fma_f32 v[80:81], v[44:45], v[194:195], 0 op_sel_hi:[1,0,0]
	s_nop 0
	v_pk_fma_f32 v[76:77], v[4:5], v[194:195], v[80:81] op_sel:[0,1,0]
	s_nop 0
	v_pk_fma_f32 v[76:77], v[46:47], v[196:197], v[76:77] op_sel_hi:[1,0,1]
	v_mov_b32_e32 v196, v197
	v_pk_fma_f32 v[80:81], v[2:3], v[196:197], v[76:77] op_sel_hi:[1,0,1]
	ds_read_b128 v[194:197], v127
	s_waitcnt lgkmcnt(3)
	v_pk_fma_f32 v[80:81], v[48:49], v[198:199], v[80:81] op_sel_hi:[1,0,1]
	s_nop 0
	v_pk_fma_f32 v[76:77], v[12:13], v[198:199], v[80:81] op_sel:[0,1,0]
	s_nop 0
	v_pk_fma_f32 v[76:77], v[50:51], v[200:201], v[76:77] op_sel_hi:[1,0,1]
	v_mov_b32_e32 v200, v201
	v_pk_fma_f32 v[80:81], v[10:11], v[200:201], v[76:77] op_sel_hi:[1,0,1]
	ds_read_b128 v[198:201], v128
	s_waitcnt lgkmcnt(3)
	v_pk_fma_f32 v[80:81], v[52:53], v[202:203], v[80:81] op_sel_hi:[1,0,1]
	s_nop 0
	v_pk_fma_f32 v[76:77], v[42:43], v[202:203], v[80:81] op_sel:[0,1,0]
	s_nop 0
	v_pk_fma_f32 v[76:77], v[54:55], v[204:205], v[76:77] op_sel_hi:[1,0,1]
	v_mov_b32_e32 v204, v205
	v_pk_fma_f32 v[80:81], v[40:41], v[204:205], v[76:77] op_sel_hi:[1,0,1]
	ds_read_b128 v[202:205], v129
	s_waitcnt lgkmcnt(3)
	v_pk_fma_f32 v[80:81], v[56:57], v[206:207], v[80:81] op_sel_hi:[1,0,1]
	s_nop 0
	v_pk_fma_f32 v[76:77], v[8:9], v[206:207], v[80:81] op_sel:[0,1,0]
	s_nop 0
	v_pk_fma_f32 v[76:77], v[58:59], v[208:209], v[76:77] op_sel_hi:[1,0,1]
	v_mov_b32_e32 v208, v209
	v_pk_fma_f32 v[76:77], v[6:7], v[208:209], v[76:77] op_sel_hi:[1,0,1]
	ds_read_b128 v[206:209], v130
	s_nop 0
	v_permlane16_swap_b32_e32 v60, v76
	v_permlane16_swap_b32_e32 v61, v77
	s_waitcnt lgkmcnt(3)
	v_pk_fma_f32 v[82:83], v[44:45], v[194:195], 0 op_sel_hi:[1,0,0]
	s_nop 0
	v_pk_fma_f32 v[78:79], v[4:5], v[194:195], v[82:83] op_sel:[0,1,0]
	s_nop 0
	v_pk_fma_f32 v[78:79], v[46:47], v[196:197], v[78:79] op_sel_hi:[1,0,1]
	v_mov_b32_e32 v196, v197
	v_pk_fma_f32 v[82:83], v[2:3], v[196:197], v[78:79] op_sel_hi:[1,0,1]
	ds_read_b128 v[194:197], v131
	s_waitcnt lgkmcnt(3)
	v_pk_fma_f32 v[82:83], v[48:49], v[198:199], v[82:83] op_sel_hi:[1,0,1]
	s_nop 0
	v_pk_fma_f32 v[78:79], v[12:13], v[198:199], v[82:83] op_sel:[0,1,0]
	s_nop 0
	v_pk_fma_f32 v[78:79], v[50:51], v[200:201], v[78:79] op_sel_hi:[1,0,1]
	v_mov_b32_e32 v200, v201
	v_pk_fma_f32 v[82:83], v[10:11], v[200:201], v[78:79] op_sel_hi:[1,0,1]
	ds_read_b128 v[198:201], v132
	s_waitcnt lgkmcnt(3)
	v_pk_fma_f32 v[82:83], v[52:53], v[202:203], v[82:83] op_sel_hi:[1,0,1]
	s_nop 0
	v_pk_fma_f32 v[78:79], v[42:43], v[202:203], v[82:83] op_sel:[0,1,0]
	s_nop 0
	v_pk_fma_f32 v[78:79], v[54:55], v[204:205], v[78:79] op_sel_hi:[1,0,1]
	v_mov_b32_e32 v204, v205
	v_pk_fma_f32 v[82:83], v[40:41], v[204:205], v[78:79] op_sel_hi:[1,0,1]
	ds_read_b128 v[202:205], v133
	s_waitcnt lgkmcnt(3)
	v_pk_fma_f32 v[82:83], v[56:57], v[206:207], v[82:83] op_sel_hi:[1,0,1]
	s_nop 0
	v_pk_fma_f32 v[78:79], v[8:9], v[206:207], v[82:83] op_sel:[0,1,0]
	s_nop 0
	v_pk_fma_f32 v[78:79], v[58:59], v[208:209], v[78:79] op_sel_hi:[1,0,1]
	v_mov_b32_e32 v208, v209
	v_pk_fma_f32 v[78:79], v[6:7], v[208:209], v[78:79] op_sel_hi:[1,0,1]
	ds_read_b128 v[206:209], v134
	s_nop 0
	v_permlane16_swap_b32_e32 v62, v78
	v_permlane16_swap_b32_e32 v63, v79
	s_waitcnt lgkmcnt(3)
	v_pk_fma_f32 v[84:85], v[44:45], v[194:195], 0 op_sel_hi:[1,0,0]
	s_nop 0
	v_pk_fma_f32 v[80:81], v[4:5], v[194:195], v[84:85] op_sel:[0,1,0]
	s_nop 0
	v_pk_fma_f32 v[80:81], v[46:47], v[196:197], v[80:81] op_sel_hi:[1,0,1]
	v_mov_b32_e32 v196, v197
	v_pk_fma_f32 v[84:85], v[2:3], v[196:197], v[80:81] op_sel_hi:[1,0,1]
	ds_read_b128 v[194:197], v135
	s_waitcnt lgkmcnt(3)
	v_pk_fma_f32 v[84:85], v[48:49], v[198:199], v[84:85] op_sel_hi:[1,0,1]
	s_nop 0
	v_pk_fma_f32 v[80:81], v[12:13], v[198:199], v[84:85] op_sel:[0,1,0]
	s_nop 0
	v_pk_fma_f32 v[80:81], v[50:51], v[200:201], v[80:81] op_sel_hi:[1,0,1]
	v_mov_b32_e32 v200, v201
	v_pk_fma_f32 v[84:85], v[10:11], v[200:201], v[80:81] op_sel_hi:[1,0,1]
	ds_read_b128 v[198:201], v136
	s_waitcnt lgkmcnt(3)
	v_pk_fma_f32 v[84:85], v[52:53], v[202:203], v[84:85] op_sel_hi:[1,0,1]
	s_nop 0
	v_pk_fma_f32 v[80:81], v[42:43], v[202:203], v[84:85] op_sel:[0,1,0]
	s_nop 0
	v_pk_fma_f32 v[80:81], v[54:55], v[204:205], v[80:81] op_sel_hi:[1,0,1]
	v_mov_b32_e32 v204, v205
	v_pk_fma_f32 v[84:85], v[40:41], v[204:205], v[80:81] op_sel_hi:[1,0,1]
	ds_read_b128 v[202:205], v137
	s_waitcnt lgkmcnt(3)
	v_pk_fma_f32 v[84:85], v[56:57], v[206:207], v[84:85] op_sel_hi:[1,0,1]
	s_nop 0
	v_pk_fma_f32 v[80:81], v[8:9], v[206:207], v[84:85] op_sel:[0,1,0]
	s_nop 0
	v_pk_fma_f32 v[80:81], v[58:59], v[208:209], v[80:81] op_sel_hi:[1,0,1]
	v_mov_b32_e32 v208, v209
	v_pk_fma_f32 v[80:81], v[6:7], v[208:209], v[80:81] op_sel_hi:[1,0,1]
	ds_read_b128 v[206:209], v138
	s_nop 0
	v_permlane16_swap_b32_e32 v64, v80
	v_permlane16_swap_b32_e32 v65, v81
	s_waitcnt lgkmcnt(3)
	v_pk_fma_f32 v[86:87], v[44:45], v[194:195], 0 op_sel_hi:[1,0,0]
	s_nop 0
	v_pk_fma_f32 v[82:83], v[4:5], v[194:195], v[86:87] op_sel:[0,1,0]
	s_nop 0
	v_pk_fma_f32 v[82:83], v[46:47], v[196:197], v[82:83] op_sel_hi:[1,0,1]
	v_mov_b32_e32 v196, v197
	v_pk_fma_f32 v[86:87], v[2:3], v[196:197], v[82:83] op_sel_hi:[1,0,1]
	ds_read_b128 v[194:197], v139
	s_waitcnt lgkmcnt(3)
	v_pk_fma_f32 v[86:87], v[48:49], v[198:199], v[86:87] op_sel_hi:[1,0,1]
	s_nop 0
	v_pk_fma_f32 v[82:83], v[12:13], v[198:199], v[86:87] op_sel:[0,1,0]
	s_nop 0
	v_pk_fma_f32 v[82:83], v[50:51], v[200:201], v[82:83] op_sel_hi:[1,0,1]
	v_mov_b32_e32 v200, v201
	v_pk_fma_f32 v[86:87], v[10:11], v[200:201], v[82:83] op_sel_hi:[1,0,1]
	ds_read_b128 v[198:201], v140
	s_waitcnt lgkmcnt(3)
	v_pk_fma_f32 v[86:87], v[52:53], v[202:203], v[86:87] op_sel_hi:[1,0,1]
	s_nop 0
	v_pk_fma_f32 v[82:83], v[42:43], v[202:203], v[86:87] op_sel:[0,1,0]
	s_nop 0
	v_pk_fma_f32 v[82:83], v[54:55], v[204:205], v[82:83] op_sel_hi:[1,0,1]
	v_mov_b32_e32 v204, v205
	v_pk_fma_f32 v[86:87], v[40:41], v[204:205], v[82:83] op_sel_hi:[1,0,1]
	ds_read_b128 v[202:205], v141
	s_waitcnt lgkmcnt(3)
	v_pk_fma_f32 v[86:87], v[56:57], v[206:207], v[86:87] op_sel_hi:[1,0,1]
	s_nop 0
	v_pk_fma_f32 v[82:83], v[8:9], v[206:207], v[86:87] op_sel:[0,1,0]
	s_nop 0
	v_pk_fma_f32 v[82:83], v[58:59], v[208:209], v[82:83] op_sel_hi:[1,0,1]
	v_mov_b32_e32 v208, v209
	v_pk_fma_f32 v[82:83], v[6:7], v[208:209], v[82:83] op_sel_hi:[1,0,1]
	ds_read_b128 v[206:209], v142
	s_nop 0
	v_permlane16_swap_b32_e32 v66, v82
	v_permlane16_swap_b32_e32 v67, v83
	s_waitcnt lgkmcnt(3)
	v_pk_fma_f32 v[168:169], v[44:45], v[194:195], 0 op_sel_hi:[1,0,0]
	s_nop 0
	v_pk_fma_f32 v[84:85], v[4:5], v[194:195], v[168:169] op_sel:[0,1,0]
	s_nop 0
	v_pk_fma_f32 v[84:85], v[46:47], v[196:197], v[84:85] op_sel_hi:[1,0,1]
	v_mov_b32_e32 v196, v197
	v_pk_fma_f32 v[168:169], v[2:3], v[196:197], v[84:85] op_sel_hi:[1,0,1]
	ds_read_b128 v[194:197], v143
	s_waitcnt lgkmcnt(3)
	v_pk_fma_f32 v[168:169], v[48:49], v[198:199], v[168:169] op_sel_hi:[1,0,1]
	s_nop 0
	v_pk_fma_f32 v[84:85], v[12:13], v[198:199], v[168:169] op_sel:[0,1,0]
	s_nop 0
	v_pk_fma_f32 v[84:85], v[50:51], v[200:201], v[84:85] op_sel_hi:[1,0,1]
	v_mov_b32_e32 v200, v201
	v_pk_fma_f32 v[168:169], v[10:11], v[200:201], v[84:85] op_sel_hi:[1,0,1]
	ds_read_b128 v[198:201], v144
	s_waitcnt lgkmcnt(3)
	v_pk_fma_f32 v[168:169], v[52:53], v[202:203], v[168:169] op_sel_hi:[1,0,1]
	s_nop 0
	v_pk_fma_f32 v[84:85], v[42:43], v[202:203], v[168:169] op_sel:[0,1,0]
	s_nop 0
	v_pk_fma_f32 v[84:85], v[54:55], v[204:205], v[84:85] op_sel_hi:[1,0,1]
	v_mov_b32_e32 v204, v205
	v_pk_fma_f32 v[168:169], v[40:41], v[204:205], v[84:85] op_sel_hi:[1,0,1]
	ds_read_b128 v[202:205], v145
	s_waitcnt lgkmcnt(3)
	v_pk_fma_f32 v[168:169], v[56:57], v[206:207], v[168:169] op_sel_hi:[1,0,1]
	s_nop 0
	v_pk_fma_f32 v[84:85], v[8:9], v[206:207], v[168:169] op_sel:[0,1,0]
	v_pk_fma_f32 v[84:85], v[58:59], v[208:209], v[84:85] op_sel_hi:[1,0,1]
	v_mov_b32_e32 v208, v209
	v_pk_fma_f32 v[84:85], v[6:7], v[208:209], v[84:85] op_sel_hi:[1,0,1]
	ds_read_b128 v[206:209], v146
	s_waitcnt lgkmcnt(3)
	v_pk_fma_f32 v[86:87], v[44:45], v[194:195], 0 op_sel_hi:[1,0,0]
	s_nop 0
	v_pk_fma_f32 v[86:87], v[4:5], v[194:195], v[86:87] op_sel:[0,1,0]
	v_mov_b32_e32 v194, v197
	v_pk_fma_f32 v[86:87], v[46:47], v[196:197], v[86:87] op_sel_hi:[1,0,1]
	v_permlane16_swap_b32_e32 v68, v84
	v_pk_fma_f32 v[86:87], v[2:3], v[194:195], v[86:87] op_sel_hi:[1,0,1]
	ds_read_b128 v[194:197], v147
	v_permlane16_swap_b32_e32 v69, v85
	s_waitcnt lgkmcnt(3)
	v_pk_fma_f32 v[86:87], v[48:49], v[198:199], v[86:87] op_sel_hi:[1,0,1]
	s_nop 0
	v_pk_fma_f32 v[86:87], v[12:13], v[198:199], v[86:87] op_sel:[0,1,0]
	v_mov_b32_e32 v198, v201
	v_pk_fma_f32 v[86:87], v[50:51], v[200:201], v[86:87] op_sel_hi:[1,0,1]
	s_nop 0
	v_pk_fma_f32 v[86:87], v[10:11], v[198:199], v[86:87] op_sel_hi:[1,0,1]
	ds_read_b128 v[198:201], v148
	s_waitcnt lgkmcnt(3)
	v_pk_fma_f32 v[86:87], v[52:53], v[202:203], v[86:87] op_sel_hi:[1,0,1]
	s_nop 0
	v_pk_fma_f32 v[86:87], v[42:43], v[202:203], v[86:87] op_sel:[0,1,0]
	v_mov_b32_e32 v202, v205
	v_pk_fma_f32 v[86:87], v[54:55], v[204:205], v[86:87] op_sel_hi:[1,0,1]
	s_nop 0
	v_pk_fma_f32 v[86:87], v[40:41], v[202:203], v[86:87] op_sel_hi:[1,0,1]
	ds_read_b128 v[202:205], v149
	s_waitcnt lgkmcnt(3)
	v_pk_fma_f32 v[86:87], v[56:57], v[206:207], v[86:87] op_sel_hi:[1,0,1]
	s_nop 0
	v_pk_fma_f32 v[86:87], v[8:9], v[206:207], v[86:87] op_sel:[0,1,0]
	v_mov_b32_e32 v206, v209
	v_pk_fma_f32 v[86:87], v[58:59], v[208:209], v[86:87] op_sel_hi:[1,0,1]
	s_nop 0
	v_pk_fma_f32 v[86:87], v[6:7], v[206:207], v[86:87] op_sel_hi:[1,0,1]
	ds_read_b128 v[206:209], v150
	s_nop 0
	v_permlane16_swap_b32_e32 v70, v86
	v_permlane16_swap_b32_e32 v71, v87
	s_waitcnt lgkmcnt(3)
	v_pk_fma_f32 v[172:173], v[44:45], v[194:195], 0 op_sel_hi:[1,0,0]
	s_nop 0
	v_pk_fma_f32 v[168:169], v[4:5], v[194:195], v[172:173] op_sel:[0,1,0]
	s_nop 0
	v_pk_fma_f32 v[168:169], v[46:47], v[196:197], v[168:169] op_sel_hi:[1,0,1]
	v_mov_b32_e32 v196, v197
	v_pk_fma_f32 v[172:173], v[2:3], v[196:197], v[168:169] op_sel_hi:[1,0,1]
	ds_read_b128 v[194:197], v151
	s_waitcnt lgkmcnt(3)
	v_pk_fma_f32 v[172:173], v[48:49], v[198:199], v[172:173] op_sel_hi:[1,0,1]
	s_nop 0
	v_pk_fma_f32 v[168:169], v[12:13], v[198:199], v[172:173] op_sel:[0,1,0]
	s_nop 0
	v_pk_fma_f32 v[168:169], v[50:51], v[200:201], v[168:169] op_sel_hi:[1,0,1]
	v_mov_b32_e32 v200, v201
	v_pk_fma_f32 v[172:173], v[10:11], v[200:201], v[168:169] op_sel_hi:[1,0,1]
	ds_read_b128 v[198:201], v152
	s_waitcnt lgkmcnt(3)
	v_pk_fma_f32 v[172:173], v[52:53], v[202:203], v[172:173] op_sel_hi:[1,0,1]
	s_nop 0
	v_pk_fma_f32 v[168:169], v[42:43], v[202:203], v[172:173] op_sel:[0,1,0]
	s_nop 0
	v_pk_fma_f32 v[168:169], v[54:55], v[204:205], v[168:169] op_sel_hi:[1,0,1]
	v_mov_b32_e32 v204, v205
	v_pk_fma_f32 v[172:173], v[40:41], v[204:205], v[168:169] op_sel_hi:[1,0,1]
	ds_read_b128 v[202:205], v153
	s_waitcnt lgkmcnt(3)
	v_pk_fma_f32 v[172:173], v[56:57], v[206:207], v[172:173] op_sel_hi:[1,0,1]
	s_nop 0
	v_pk_fma_f32 v[168:169], v[8:9], v[206:207], v[172:173] op_sel:[0,1,0]
	s_nop 0
	v_pk_fma_f32 v[168:169], v[58:59], v[208:209], v[168:169] op_sel_hi:[1,0,1]
	v_mov_b32_e32 v208, v209
	v_pk_fma_f32 v[172:173], v[6:7], v[208:209], v[168:169] op_sel_hi:[1,0,1]
	ds_read_b128 v[206:209], v154
	s_nop 0
	v_permlane16_swap_b32_e32 v72, v172
	v_permlane16_swap_b32_e32 v73, v173
	s_waitcnt lgkmcnt(3)
	v_pk_fma_f32 v[44:45], v[44:45], v[194:195], 0 op_sel_hi:[1,0,0]
	s_nop 0
	v_pk_fma_f32 v[4:5], v[4:5], v[194:195], v[44:45] op_sel:[0,1,0]
	v_mov_b32_e32 v44, v197
	v_pk_fma_f32 v[4:5], v[46:47], v[196:197], v[4:5] op_sel_hi:[1,0,1]
	s_nop 0
	v_pk_fma_f32 v[44:45], v[2:3], v[44:45], v[4:5] op_sel_hi:[1,0,1]
	s_waitcnt lgkmcnt(2)
	v_pk_fma_f32 v[44:45], v[48:49], v[198:199], v[44:45] op_sel_hi:[1,0,1]
	s_nop 0
	v_pk_fma_f32 v[2:3], v[12:13], v[198:199], v[44:45] op_sel:[0,1,0]
	s_nop 0
	v_pk_fma_f32 v[2:3], v[50:51], v[200:201], v[2:3] op_sel_hi:[1,0,1]
	v_mov_b32_e32 v200, v201
	v_pk_fma_f32 v[10:11], v[10:11], v[200:201], v[2:3] op_sel_hi:[1,0,1]
	s_waitcnt lgkmcnt(1)
	v_pk_fma_f32 v[10:11], v[52:53], v[202:203], v[10:11] op_sel_hi:[1,0,1]
	s_nop 0
	v_pk_fma_f32 v[2:3], v[42:43], v[202:203], v[10:11] op_sel:[0,1,0]
	s_nop 0
	v_pk_fma_f32 v[2:3], v[54:55], v[204:205], v[2:3] op_sel_hi:[1,0,1]
	v_mov_b32_e32 v204, v205
	v_pk_fma_f32 v[10:11], v[40:41], v[204:205], v[2:3] op_sel_hi:[1,0,1]
	s_waitcnt lgkmcnt(0)
	v_pk_fma_f32 v[10:11], v[56:57], v[206:207], v[10:11] op_sel_hi:[1,0,1]
	s_nop 0
	v_pk_fma_f32 v[2:3], v[8:9], v[206:207], v[10:11] op_sel:[0,1,0]
	v_add_f32_e32 v8, v68, v84
	v_pk_fma_f32 v[2:3], v[58:59], v[208:209], v[2:3] op_sel_hi:[1,0,1]
	v_mov_b32_e32 v208, v209
	v_pk_fma_f32 v[2:3], v[6:7], v[208:209], v[2:3] op_sel_hi:[1,0,1]
	v_add_f32_e32 v4, v60, v76
	v_add_f32_e32 v5, v62, v78
	v_add_f32_e32 v9, v70, v86
	v_add_f32_e32 v6, v64, v80
	v_add_f32_e32 v10, v72, v172
	v_permlane16_swap_b32_e32 v74, v2
	v_cndmask_b32_e64 v11, v4, v8, s[40:41]
	v_cndmask_b32_e64 v4, v8, v4, s[40:41]
	v_cndmask_b32_e64 v8, v5, v9, s[40:41]
	v_cndmask_b32_e64 v5, v9, v5, s[40:41]
	v_add_f32_e32 v7, v66, v82
	v_add_f32_e32 v2, v74, v2
	v_add_f32_dpp v5, v8, v5 row_mirror row_mask:0xf bank_mask:0xf bound_ctrl:1
	v_cndmask_b32_e64 v8, v6, v10, s[40:41]
	v_cndmask_b32_e64 v6, v10, v6, s[40:41]
	v_add_f32_dpp v4, v11, v4 row_mirror row_mask:0xf bank_mask:0xf bound_ctrl:1
	v_add_f32_e32 v9, v71, v87
	v_add_f32_dpp v6, v8, v6 row_mirror row_mask:0xf bank_mask:0xf bound_ctrl:1
	v_cndmask_b32_e64 v8, v7, v2, s[40:41]
	v_cndmask_b32_e64 v2, v2, v7, s[40:41]
	v_cndmask_b32_e64 v7, v4, v6, s[42:43]
	v_cndmask_b32_e64 v4, v6, v4, s[42:43]
	v_add_f32_dpp v2, v8, v2 row_mirror row_mask:0xf bank_mask:0xf bound_ctrl:1
	v_cndmask_b32_e64 v6, v5, v2, s[42:43]
	v_cndmask_b32_e64 v2, v2, v5, s[42:43]
	v_add_f32_dpp v4, v7, v4 row_half_mirror row_mask:0xf bank_mask:0xf bound_ctrl:1
	v_add_f32_e32 v8, v69, v85
	v_add_f32_dpp v2, v6, v2 row_half_mirror row_mask:0xf bank_mask:0xf bound_ctrl:1
	v_cndmask_b32_e64 v5, v4, v2, s[44:45]
	v_cndmask_b32_e64 v2, v2, v4, s[44:45]
	v_add_f32_e32 v6, v65, v81
	v_add_f32_e32 v10, v73, v173
	v_add_f32_dpp v2, v5, v2 quad_perm:[2,3,0,1] row_mask:0xf bank_mask:0xf bound_ctrl:1
	v_add_f32_e32 v5, v63, v79
	v_permlane16_swap_b32_e32 v75, v3
	v_add_f32_dpp v2, v2, v2 quad_perm:[1,0,3,2] row_mask:0xf bank_mask:0xf bound_ctrl:1
	v_mov_b32_e32 v4, v2
	s_nop 1
	v_permlane32_swap_b32_e32 v2, v4
	v_add_f32_e32 v2, v2, v4
	v_add_f32_e32 v4, v61, v77
	v_cndmask_b32_e64 v11, v4, v8, s[40:41]
	v_cndmask_b32_e64 v4, v8, v4, s[40:41]
	v_cndmask_b32_e64 v8, v5, v9, s[40:41]
	v_cndmask_b32_e64 v5, v9, v5, s[40:41]
	v_add_f32_e32 v7, v67, v83
	v_add_f32_e32 v3, v75, v3
	v_add_f32_dpp v5, v8, v5 row_mirror row_mask:0xf bank_mask:0xf bound_ctrl:1
	v_cndmask_b32_e64 v8, v6, v10, s[40:41]
	v_cndmask_b32_e64 v6, v10, v6, s[40:41]
	v_add_f32_dpp v4, v11, v4 row_mirror row_mask:0xf bank_mask:0xf bound_ctrl:1
	v_cndmask_b32_e64 v2, v2, v166, s[48:49]
	v_add_f32_dpp v6, v8, v6 row_mirror row_mask:0xf bank_mask:0xf bound_ctrl:1
	v_cndmask_b32_e64 v8, v7, v3, s[40:41]
	v_cndmask_b32_e64 v3, v3, v7, s[40:41]
	v_cndmask_b32_e64 v7, v4, v6, s[42:43]
	v_cndmask_b32_e64 v4, v6, v4, s[42:43]
	v_add_f32_dpp v3, v8, v3 row_mirror row_mask:0xf bank_mask:0xf bound_ctrl:1
	v_cndmask_b32_e64 v6, v5, v3, s[42:43]
	v_cndmask_b32_e64 v3, v3, v5, s[42:43]
	v_add_f32_dpp v4, v7, v4 row_half_mirror row_mask:0xf bank_mask:0xf bound_ctrl:1
	v_add_f32_e32 v2, v88, v2
	v_add_f32_dpp v3, v6, v3 row_half_mirror row_mask:0xf bank_mask:0xf bound_ctrl:1
	v_cndmask_b32_e64 v5, v4, v3, s[44:45]
	v_cndmask_b32_e64 v3, v3, v4, s[44:45]
	s_nop 1
	v_add_f32_dpp v3, v5, v3 quad_perm:[2,3,0,1] row_mask:0xf bank_mask:0xf bound_ctrl:1
	v_mov_b32_dpp v5, v2 quad_perm:[1,0,3,2] row_mask:0xf bank_mask:0xf bound_ctrl:1
	v_max_f32_e32 v5, v5, v5
	v_max_f32_e32 v5, v2, v5
	v_add_f32_dpp v3, v3, v3 quad_perm:[1,0,3,2] row_mask:0xf bank_mask:0xf bound_ctrl:1
	v_mov_b32_e32 v4, v3
	v_mov_b32_dpp v6, v5 quad_perm:[2,3,0,1] row_mask:0xf bank_mask:0xf bound_ctrl:1
	v_max_f32_e32 v6, v6, v6
	v_max_f32_e32 v5, v5, v6
	v_permlane32_swap_b32_e32 v3, v4
	s_nop 0
	v_mov_b32_dpp v6, v5 row_half_mirror row_mask:0xf bank_mask:0xf bound_ctrl:1
	v_max_f32_e32 v6, v6, v6
	v_max_f32_e32 v5, v5, v6
	s_nop 1
	v_mov_b32_dpp v6, v5 row_mirror row_mask:0xf bank_mask:0xf bound_ctrl:1
	v_max_f32_e32 v6, v6, v6
	v_max_f32_e32 v5, v5, v6
	v_mov_b32_e32 v6, v5
	s_nop 1
	v_permlane16_swap_b32_e32 v5, v6
	v_max_f32_e32 v6, v6, v6
	v_max_f32_e32 v5, v5, v5
	v_max_f32_e32 v5, v5, v6
	v_mov_b32_e32 v6, v5
	s_nop 1
	v_permlane32_swap_b32_e32 v5, v6
	v_max_f32_e32 v6, v6, v6
	v_max_f32_e32 v5, v5, v5
	v_max_f32_e32 v5, v5, v6
	v_cmp_eq_f32_e32 vcc, v2, v5
	s_ff1_i32_b64 s0, vcc
	s_lshr_b32 s0, s0, 1
	s_cmp_lg_u64 vcc, 0
	s_cselect_b32 s7, s0, -1
	v_cmp_ne_u32_e32 vcc, s7, v1
	s_nop 1
	v_cndmask_b32_e32 v2, v221, v2, vcc
	s_nop 1
	v_mov_b32_dpp v6, v2 quad_perm:[1,0,3,2] row_mask:0xf bank_mask:0xf bound_ctrl:1
	v_max_f32_e32 v6, v6, v6
	v_max_f32_e32 v6, v2, v6
	s_nop 1
	v_mov_b32_dpp v7, v6 quad_perm:[2,3,0,1] row_mask:0xf bank_mask:0xf bound_ctrl:1
	v_max_f32_e32 v7, v7, v7
	v_max_f32_e32 v6, v6, v7
	s_nop 1
	v_mov_b32_dpp v7, v6 row_half_mirror row_mask:0xf bank_mask:0xf bound_ctrl:1
	v_max_f32_e32 v7, v7, v7
	v_max_f32_e32 v6, v6, v7
	s_nop 1
	v_mov_b32_dpp v7, v6 row_mirror row_mask:0xf bank_mask:0xf bound_ctrl:1
	v_max_f32_e32 v7, v7, v7
	v_max_f32_e32 v6, v6, v7
	v_mov_b32_e32 v7, v6
	s_nop 1
	v_permlane16_swap_b32_e32 v6, v7
	v_max_f32_e32 v7, v7, v7
	v_max_f32_e32 v6, v6, v6
	v_max_f32_e32 v6, v6, v7
	v_mov_b32_e32 v7, v6
	s_nop 1
	v_permlane32_swap_b32_e32 v6, v7
	v_max_f32_e32 v7, v7, v7
	v_max_f32_e32 v6, v6, v6
	v_max_f32_e32 v6, v6, v7
	v_cmp_eq_f32_e32 vcc, v2, v6
	s_ff1_i32_b64 s0, vcc
	s_lshr_b32 s0, s0, 1
	s_cmp_lg_u64 vcc, 0
	s_cselect_b32 s14, s0, -1
	v_cmp_ne_u32_e32 vcc, s14, v1
	s_nop 1
	v_cndmask_b32_e32 v2, v221, v2, vcc
	s_nop 1
	v_mov_b32_dpp v7, v2 quad_perm:[1,0,3,2] row_mask:0xf bank_mask:0xf bound_ctrl:1
	v_max_f32_e32 v7, v7, v7
	v_max_f32_e32 v7, v2, v7
	s_nop 1
	v_mov_b32_dpp v8, v7 quad_perm:[2,3,0,1] row_mask:0xf bank_mask:0xf bound_ctrl:1
	v_max_f32_e32 v8, v8, v8
	v_max_f32_e32 v7, v7, v8
	s_nop 1
	v_mov_b32_dpp v8, v7 row_half_mirror row_mask:0xf bank_mask:0xf bound_ctrl:1
	v_max_f32_e32 v8, v8, v8
	v_max_f32_e32 v7, v7, v8
	s_nop 1
	v_mov_b32_dpp v8, v7 row_mirror row_mask:0xf bank_mask:0xf bound_ctrl:1
	v_max_f32_e32 v8, v8, v8
	v_max_f32_e32 v7, v7, v8
	v_mov_b32_e32 v8, v7
	s_nop 1
	v_permlane16_swap_b32_e32 v7, v8
	v_max_f32_e32 v8, v8, v8
	v_max_f32_e32 v7, v7, v7
	v_max_f32_e32 v7, v7, v8
	v_mov_b32_e32 v8, v7
	s_nop 1
	v_permlane32_swap_b32_e32 v7, v8
	v_max_f32_e32 v8, v8, v8
	v_max_f32_e32 v7, v7, v7
	v_max_f32_e32 v7, v7, v8
	v_cmp_eq_f32_e32 vcc, v2, v7
	s_ff1_i32_b64 s0, vcc
	s_lshr_b32 s0, s0, 1
	s_cmp_lg_u64 vcc, 0
	s_cselect_b32 s15, s0, -1
	v_cmp_ne_u32_e32 vcc, s15, v1
	s_nop 1
	v_cndmask_b32_e32 v2, v221, v2, vcc
	s_nop 1
	v_mov_b32_dpp v8, v2 quad_perm:[1,0,3,2] row_mask:0xf bank_mask:0xf bound_ctrl:1
	v_max_f32_e32 v8, v8, v8
	v_max_f32_e32 v8, v2, v8
	s_nop 1
	v_mov_b32_dpp v9, v8 quad_perm:[2,3,0,1] row_mask:0xf bank_mask:0xf bound_ctrl:1
	v_max_f32_e32 v9, v9, v9
	v_max_f32_e32 v8, v8, v9
	s_nop 1
	v_mov_b32_dpp v9, v8 row_half_mirror row_mask:0xf bank_mask:0xf bound_ctrl:1
	v_max_f32_e32 v9, v9, v9
	v_max_f32_e32 v8, v8, v9
	s_nop 1
	v_mov_b32_dpp v9, v8 row_mirror row_mask:0xf bank_mask:0xf bound_ctrl:1
	v_max_f32_e32 v9, v9, v9
	v_max_f32_e32 v8, v8, v9
	v_mov_b32_e32 v9, v8
	s_nop 1
	v_permlane16_swap_b32_e32 v8, v9
	v_max_f32_e32 v9, v9, v9
	v_max_f32_e32 v8, v8, v8
	v_max_f32_e32 v8, v8, v9
	v_mov_b32_e32 v9, v8
	s_nop 1
	v_permlane32_swap_b32_e32 v8, v9
	v_max_f32_e32 v9, v9, v9
	v_max_f32_e32 v8, v8, v8
	v_max_f32_e32 v8, v8, v9
	v_cmp_eq_f32_e64 s[0:1], v2, v8
	v_add_u32_e32 v2, s27, v159
	s_and_saveexec_b64 s[12:13], s[50:51]
	s_cbranch_execz .LBB0_1366
	v_sub_f32_e32 v6, v6, v5
	v_mul_f32_e32 v6, 0x3fb8aa3b, v6
	v_sub_f32_e32 v7, v7, v5
	v_exp_f32_e32 v6, v6
	v_mul_f32_e32 v7, 0x3fb8aa3b, v7
	v_sub_f32_e32 v5, v8, v5
	v_exp_f32_e32 v7, v7
	v_mul_f32_e32 v5, 0x3fb8aa3b, v5
	v_exp_f32_e32 v5, v5
	v_add_f32_e32 v8, 1.0, v6
	v_add_f32_e32 v8, v8, v7
	v_add_f32_e32 v8, v8, v5
	v_div_scale_f32 v9, s[28:29], v8, v8, 1.0
	v_rcp_f32_e32 v10, v9
	s_ff1_i32_b64 s28, s[0:1]
	s_lshr_b32 s28, s28, 1
	s_cmp_lg_u64 s[0:1], 0
	v_fma_f32 v11, -v9, v10, 1.0
	v_fmac_f32_e32 v10, v11, v10
	v_div_scale_f32 v11, vcc, 1.0, v8, 1.0
	v_mul_f32_e32 v12, v11, v10
	v_fma_f32 v13, -v9, v12, v11
	v_fmac_f32_e32 v12, v13, v10
	v_fma_f32 v9, -v9, v12, v11
	v_div_fmas_f32 v9, v9, v10, v12
	s_cselect_b32 s0, s28, -1
	v_cndmask_b32_e64 v5, v5, v7, s[56:57]
	v_div_fixup_f32 v8, v9, v8, 1.0
	v_mov_b32_e32 v9, s0
	v_mov_b32_e32 v10, s15
	v_cndmask_b32_e64 v5, v5, v6, s[54:55]
	v_cndmask_b32_e64 v9, v9, v10, s[56:57]
	v_mov_b32_e32 v10, s14
	v_cndmask_b32_e64 v5, v5, 1.0, s[52:53]
	v_cndmask_b32_e64 v9, v9, v10, s[54:55]
	v_mov_b32_e32 v10, s7
	v_mul_f32_e32 v5, v8, v5
	v_lshl_add_u64 v[6:7], s[8:9], 4, v[18:19]
	v_cndmask_b32_e64 v9, v9, v10, s[52:53]
	global_store_dword v[6:7], v5, off
	v_add_u32_e32 v5, 0x22300, v2
	ds_write_b32 v5, v9
	v_lshl_add_u32 v5, v9, 2, 0
	v_add_u32_e32 v5, 0x22200, v5
	ds_add_rtn_u32 v5, v5, v210
	v_add_u32_e32 v6, 0x22700, v2
	s_waitcnt lgkmcnt(0)
	ds_write_b32 v6, v5
